# one static s_setprio 1 for waves 4-7 before the main loop, every per-phase priority flip deleted (section 7.4 recipe)
# speedup vs baseline: 1.0036x; 1.0036x over previous
.LBB2_32:
	s_xor_b64 s[30:31], s[4:5], -1
	s_lshl_b32 s4, s63, 8
	s_ashr_i32 s5, s4, 31
	s_lshl_b64 s[4:5], s[4:5], 11
	s_add_u32 s4, s14, s4
	s_addc_u32 s5, s15, s5
	s_add_u32 s24, s4, 0x400000
	s_addc_u32 s25, s5, 0
	s_and_b64 s[4:5], s[28:29], exec
	s_cselect_b32 s66, s25, s19
	s_cselect_b32 s67, s24, s18
	s_lshl_b32 s4, s62, 8
	s_ashr_i32 s5, s4, 31
	s_lshl_b64 s[4:5], s[4:5], 11
	s_add_u32 s26, s12, s4
	s_addc_u32 s27, s13, s5
	s_and_b64 s[4:5], s[28:29], exec
	s_cselect_b32 s68, s27, s1
	s_cselect_b32 s69, s26, s0
	s_add_u32 s70, s18, 0x40080
	s_addc_u32 s71, s19, 0
	s_add_u32 s72, s0, 0x100
	v_mov_b64_e32 v[0:1], 0
	s_addc_u32 s73, s1, 0
	s_mov_b32 s74, -2
	v_mov_b64_e32 v[2:3], 0
	v_mov_b64_e32 v[4:5], 0
	v_mov_b64_e32 v[6:7], 0
	v_mov_b64_e32 v[8:9], 0
	v_mov_b64_e32 v[10:11], 0
	v_mov_b64_e32 v[12:13], 0
	v_mov_b64_e32 v[14:15], 0
	v_mov_b64_e32 v[16:17], 0
	v_mov_b64_e32 v[18:19], 0
	v_mov_b64_e32 v[20:21], 0
	v_mov_b64_e32 v[22:23], 0
	v_mov_b64_e32 v[24:25], 0
	v_mov_b64_e32 v[26:27], 0
	v_mov_b64_e32 v[28:29], 0
	v_mov_b64_e32 v[30:31], 0
	v_mov_b64_e32 v[32:33], 0
	v_mov_b64_e32 v[34:35], 0
	v_mov_b64_e32 v[36:37], 0
	v_mov_b64_e32 v[38:39], 0
	v_mov_b64_e32 v[40:41], 0
	v_mov_b64_e32 v[42:43], 0
	v_mov_b64_e32 v[44:45], 0
	v_mov_b64_e32 v[46:47], 0
	v_mov_b64_e32 v[48:49], 0
	v_mov_b64_e32 v[50:51], 0
	v_mov_b64_e32 v[52:53], 0
	v_mov_b64_e32 v[54:55], 0
	v_mov_b64_e32 v[56:57], 0
	v_mov_b64_e32 v[58:59], 0
	v_mov_b64_e32 v[60:61], 0
	v_mov_b64_e32 v[62:63], 0
	v_mov_b64_e32 v[64:65], 0
	v_mov_b64_e32 v[66:67], 0
	v_mov_b64_e32 v[68:69], 0
	v_mov_b64_e32 v[70:71], 0
	v_mov_b64_e32 v[72:73], 0
	v_mov_b64_e32 v[74:75], 0
	v_mov_b64_e32 v[76:77], 0
	v_mov_b64_e32 v[78:79], 0
	v_mov_b64_e32 v[80:81], 0
	v_mov_b64_e32 v[82:83], 0
	v_mov_b64_e32 v[84:85], 0
	v_mov_b64_e32 v[86:87], 0
	v_mov_b64_e32 v[88:89], 0
	v_mov_b64_e32 v[90:91], 0
	v_mov_b64_e32 v[92:93], 0
	v_mov_b64_e32 v[94:95], 0
	v_mov_b64_e32 v[96:97], 0
	v_mov_b64_e32 v[98:99], 0
	v_mov_b64_e32 v[100:101], 0
	v_mov_b64_e32 v[102:103], 0
	v_mov_b64_e32 v[104:105], 0
	v_mov_b64_e32 v[106:107], 0
	v_mov_b64_e32 v[108:109], 0
	v_mov_b64_e32 v[110:111], 0
	v_mov_b64_e32 v[112:113], 0
	v_mov_b64_e32 v[114:115], 0
	v_mov_b64_e32 v[116:117], 0
	v_mov_b64_e32 v[118:119], 0
	v_mov_b64_e32 v[120:121], 0
	v_mov_b64_e32 v[122:123], 0
	v_mov_b64_e32 v[124:125], 0
	v_mov_b64_e32 v[126:127], 0
	s_waitcnt lgkmcnt(0)
	v_add_u32_e32 v212, 0x1c000, v199
	v_add_u32_e32 v213, 0x1c000, v200
	s_cmpk_lt_u32 s33, 0x100
	s_cbranch_scc1 .Lp1_prio_done
	s_setprio 1
.Lp1_prio_done:
	s_branch .LBB2_34
.LBB2_33:
	s_waitcnt vmcnt(6)
	s_barrier
	v_mfma_i32_16x16x64_i8 v[48:51], v[144:147], v[184:187], v[48:51]
	s_add_i32 s74, s74, 2
	v_mfma_i32_16x16x64_i8 v[40:43], v[148:151], v[184:187], v[40:43]
	s_add_u32 s70, s70, 0x100
	s_addc_u32 s71, s71, 0
	v_mfma_i32_16x16x64_i8 v[32:35], v[144:147], v[172:175], v[32:35]
	s_add_u32 s72, s72, 0x100
	s_addc_u32 s73, s73, 0
	v_mfma_i32_16x16x64_i8 v[24:27], v[148:151], v[172:175], v[24:27]
	s_cmp_gt_u32 s74, 13
	v_mfma_i32_16x16x64_i8 v[16:19], v[144:147], v[168:171], v[16:19]
	v_mfma_i32_16x16x64_i8 v[8:11], v[148:151], v[168:171], v[8:11]
	v_mfma_i32_16x16x64_i8 v[4:7], v[144:147], v[160:163], v[4:7]
	v_mfma_i32_16x16x64_i8 v[0:3], v[148:151], v[160:163], v[0:3]
	v_mfma_i32_16x16x64_i8 v[48:51], v[156:159], v[188:191], v[48:51]
	v_mfma_i32_16x16x64_i8 v[40:43], v[152:155], v[188:191], v[40:43]
	v_mfma_i32_16x16x64_i8 v[32:35], v[156:159], v[176:179], v[32:35]
	v_mfma_i32_16x16x64_i8 v[24:27], v[152:155], v[176:179], v[24:27]
	v_mfma_i32_16x16x64_i8 v[16:19], v[156:159], v[180:183], v[16:19]
	v_mfma_i32_16x16x64_i8 v[8:11], v[152:155], v[180:183], v[8:11]
	v_mfma_i32_16x16x64_i8 v[4:7], v[156:159], v[164:167], v[4:7]
	v_mfma_i32_16x16x64_i8 v[0:3], v[152:155], v[164:167], v[0:3]
	s_barrier
	s_cbranch_scc1 .LBB2_50
.LBB2_34:
	ds_read_b128 v[144:147], v203
	ds_read_b128 v[148:151], v203 offset:2048
	ds_read_b128 v[156:159], v204
	ds_read_b128 v[152:155], v204 offset:2048
	s_cmp_lg_u32 s74, 12
	s_cselect_b64 s[0:1], -1, 0
	s_and_b64 s[4:5], s[0:1], exec
	s_cselect_b32 s75, s73, s68
	s_cselect_b32 s16, s72, s69
	s_mov_b32 m0, s53
	s_and_b32 s5, s71, 0xffff
	s_mov_b32 s4, s70
	ds_read_b128 v[184:187], v205
	ds_read_b128 v[172:175], v205 offset:2048
	ds_read_b128 v[188:191], v206
	ds_read_b128 v[176:179], v206 offset:2048
	ds_read_b128 v[168:171], v205 offset:4096
	ds_read_b128 v[160:163], v205 offset:6144
	ds_read_b128 v[180:183], v206 offset:4096
	ds_read_b128 v[164:167], v206 offset:6144
	buffer_load_dwordx4 v193, s[4:7], 0 offen lds
	s_mov_b32 m0, s54
	s_or_b64 s[36:37], s[28:29], s[0:1]
	buffer_load_dwordx4 v197, s[4:7], 0 offen lds
	s_waitcnt lgkmcnt(8)
	s_barrier
	s_waitcnt lgkmcnt(0)
	v_mfma_i32_16x16x64_i8 v[124:127], v[144:147], v[184:187], v[124:127]
	s_xor_b64 s[34:35], s[36:37], -1
	v_mfma_i32_16x16x64_i8 v[120:123], v[148:151], v[184:187], v[120:123]
	v_mfma_i32_16x16x64_i8 v[108:111], v[144:147], v[172:175], v[108:111]
	v_mfma_i32_16x16x64_i8 v[104:107], v[148:151], v[172:175], v[104:107]
	v_mfma_i32_16x16x64_i8 v[96:99], v[144:147], v[168:171], v[96:99]
	v_mfma_i32_16x16x64_i8 v[88:91], v[148:151], v[168:171], v[88:91]
	v_mfma_i32_16x16x64_i8 v[80:83], v[144:147], v[160:163], v[80:83]
	v_mfma_i32_16x16x64_i8 v[72:75], v[148:151], v[160:163], v[72:75]
	v_mfma_i32_16x16x64_i8 v[124:127], v[156:159], v[188:191], v[124:127]
	v_mfma_i32_16x16x64_i8 v[120:123], v[152:155], v[188:191], v[120:123]
	v_mfma_i32_16x16x64_i8 v[108:111], v[156:159], v[176:179], v[108:111]
	v_mfma_i32_16x16x64_i8 v[104:107], v[152:155], v[176:179], v[104:107]
	v_mfma_i32_16x16x64_i8 v[96:99], v[156:159], v[180:183], v[96:99]
	v_mfma_i32_16x16x64_i8 v[88:91], v[152:155], v[180:183], v[88:91]
	v_mfma_i32_16x16x64_i8 v[80:83], v[156:159], v[164:167], v[80:83]
	v_mfma_i32_16x16x64_i8 v[72:75], v[152:155], v[164:167], v[72:75]
	s_barrier
	ds_read_b128 v[128:131], v207
	ds_read_b128 v[132:135], v207 offset:2048
	ds_read_b128 v[140:143], v208
	ds_read_b128 v[136:139], v208 offset:2048
	s_and_b64 vcc, exec, s[34:35]
	s_cbranch_vccnz .LBB2_36
	s_and_b32 s17, s75, 0xffff
	s_mov_b32 s18, s6
	s_mov_b32 s19, s7
	s_mov_b32 m0, s39
	s_nop 0
	buffer_load_dwordx4 v196, s[16:19], 0 offen lds
	s_mov_b32 m0, s40
	s_nop 0
	buffer_load_dwordx4 v198, s[16:19], 0 offen lds
.LBB2_36:
	s_add_u32 s4, s70, 0xfffc0080
	s_addc_u32 s5, s71, -1
	s_barrier
	s_waitcnt lgkmcnt(0)
	v_mfma_i32_16x16x64_i8 v[116:119], v[128:131], v[184:187], v[116:119]
	s_and_b64 s[0:1], s[0:1], exec
	s_cselect_b32 s17, s5, s66
	s_cselect_b32 s4, s4, s67
	v_mfma_i32_16x16x64_i8 v[112:115], v[132:135], v[184:187], v[112:115]
	v_mfma_i32_16x16x64_i8 v[100:103], v[128:131], v[172:175], v[100:103]
	v_mfma_i32_16x16x64_i8 v[92:95], v[132:135], v[172:175], v[92:95]
	v_mfma_i32_16x16x64_i8 v[84:87], v[128:131], v[168:171], v[84:87]
	v_mfma_i32_16x16x64_i8 v[76:79], v[132:135], v[168:171], v[76:79]
	v_mfma_i32_16x16x64_i8 v[68:71], v[128:131], v[160:163], v[68:71]
	v_mfma_i32_16x16x64_i8 v[64:67], v[132:135], v[160:163], v[64:67]
	v_mfma_i32_16x16x64_i8 v[116:119], v[140:143], v[188:191], v[116:119]
	v_mfma_i32_16x16x64_i8 v[112:115], v[136:139], v[188:191], v[112:115]
	v_mfma_i32_16x16x64_i8 v[100:103], v[140:143], v[176:179], v[100:103]
	v_mfma_i32_16x16x64_i8 v[92:95], v[136:139], v[176:179], v[92:95]
	v_mfma_i32_16x16x64_i8 v[84:87], v[140:143], v[180:183], v[84:87]
	v_mfma_i32_16x16x64_i8 v[76:79], v[136:139], v[180:183], v[76:79]
	v_mfma_i32_16x16x64_i8 v[68:71], v[140:143], v[164:167], v[68:71]
	v_mfma_i32_16x16x64_i8 v[64:67], v[136:139], v[164:167], v[64:67]
	s_barrier
	ds_read_b128 v[184:187], v205 offset:16384
	ds_read_b128 v[172:175], v205 offset:18432
	ds_read_b128 v[188:191], v206 offset:16384
	ds_read_b128 v[176:179], v206 offset:18432
	ds_read_b128 v[168:171], v205 offset:20480
	ds_read_b128 v[160:163], v205 offset:22528
	ds_read_b128 v[180:183], v206 offset:20480
	ds_read_b128 v[164:167], v206 offset:22528
	v_cndmask_b32_e64 v194, 0, 1, s[36:37]
	v_cmp_ne_u32_e64 s[0:1], 1, v194
	s_andn2_b64 vcc, exec, s[36:37]
	s_cbranch_vccnz .LBB2_38
	s_and_b32 s5, s17, 0xffff
	s_mov_b32 m0, s38
	s_nop 0
	buffer_load_dwordx4 v193, s[4:7], 0 offen lds
	s_mov_b32 m0, s41
	s_nop 0
	buffer_load_dwordx4 v197, s[4:7], 0 offen lds
.LBB2_38:
	s_barrier
	s_waitcnt lgkmcnt(0)
	v_mfma_i32_16x16x64_i8 v[60:63], v[144:147], v[184:187], v[60:63]
	v_mfma_i32_16x16x64_i8 v[56:59], v[148:151], v[184:187], v[56:59]
	v_mfma_i32_16x16x64_i8 v[52:55], v[144:147], v[172:175], v[52:55]
	v_mfma_i32_16x16x64_i8 v[44:47], v[148:151], v[172:175], v[44:47]
	v_mfma_i32_16x16x64_i8 v[36:39], v[144:147], v[168:171], v[36:39]
	v_mfma_i32_16x16x64_i8 v[28:31], v[148:151], v[168:171], v[28:31]
	v_mfma_i32_16x16x64_i8 v[20:23], v[144:147], v[160:163], v[20:23]
	v_mfma_i32_16x16x64_i8 v[12:15], v[148:151], v[160:163], v[12:15]
	v_mfma_i32_16x16x64_i8 v[60:63], v[156:159], v[188:191], v[60:63]
	v_mfma_i32_16x16x64_i8 v[56:59], v[152:155], v[188:191], v[56:59]
	v_mfma_i32_16x16x64_i8 v[52:55], v[156:159], v[176:179], v[52:55]
	v_mfma_i32_16x16x64_i8 v[44:47], v[152:155], v[176:179], v[44:47]
	v_mfma_i32_16x16x64_i8 v[36:39], v[156:159], v[180:183], v[36:39]
	v_mfma_i32_16x16x64_i8 v[28:31], v[152:155], v[180:183], v[28:31]
	v_mfma_i32_16x16x64_i8 v[20:23], v[156:159], v[164:167], v[20:23]
	v_mfma_i32_16x16x64_i8 v[12:15], v[152:155], v[164:167], v[12:15]
	s_barrier
	s_mov_b64 s[18:19], -1
	s_and_b64 vcc, exec, s[34:35]
	s_cbranch_vccz .LBB2_40
	s_waitcnt vmcnt(0)
	s_mov_b64 s[18:19], 0

.LBB2_42:
	s_barrier
	v_mfma_i32_16x16x64_i8 v[48:51], v[128:131], v[184:187], v[48:51]
	s_add_i32 s5, 0, 0x18000
	v_add_u32_e32 v210, s5, v199
	v_mfma_i32_16x16x64_i8 v[40:43], v[132:135], v[184:187], v[40:43]
	v_add_u32_e32 v211, s5, v200
	v_mfma_i32_16x16x64_i8 v[32:35], v[128:131], v[172:175], v[32:35]
	v_mfma_i32_16x16x64_i8 v[24:27], v[132:135], v[172:175], v[24:27]
	v_mfma_i32_16x16x64_i8 v[16:19], v[128:131], v[168:171], v[16:19]
	v_mfma_i32_16x16x64_i8 v[8:11], v[132:135], v[168:171], v[8:11]
	v_mfma_i32_16x16x64_i8 v[4:7], v[128:131], v[160:163], v[4:7]
	v_mfma_i32_16x16x64_i8 v[0:3], v[132:135], v[160:163], v[0:3]
	v_mfma_i32_16x16x64_i8 v[48:51], v[140:143], v[188:191], v[48:51]
	v_mfma_i32_16x16x64_i8 v[40:43], v[136:139], v[188:191], v[40:43]
	v_mfma_i32_16x16x64_i8 v[32:35], v[140:143], v[176:179], v[32:35]
	v_mfma_i32_16x16x64_i8 v[24:27], v[136:139], v[176:179], v[24:27]
	v_mfma_i32_16x16x64_i8 v[16:19], v[140:143], v[180:183], v[16:19]
	v_mfma_i32_16x16x64_i8 v[8:11], v[136:139], v[180:183], v[8:11]
	v_mfma_i32_16x16x64_i8 v[4:7], v[140:143], v[164:167], v[4:7]
	v_mfma_i32_16x16x64_i8 v[0:3], v[136:139], v[164:167], v[0:3]
	s_barrier
	ds_read_b128 v[128:131], v210
	ds_read_b128 v[132:135], v210 offset:2048
	ds_read_b128 v[140:143], v211
	ds_read_b128 v[136:139], v211 offset:2048
	ds_read_b128 v[184:187], v205 offset:32768
	ds_read_b128 v[172:175], v205 offset:34816
	ds_read_b128 v[188:191], v206 offset:32768
	ds_read_b128 v[176:179], v206 offset:34816
	ds_read_b128 v[168:171], v205 offset:36864
	ds_read_b128 v[160:163], v205 offset:38912
	ds_read_b128 v[180:183], v206 offset:36864
	ds_read_b128 v[164:167], v206 offset:38912
	s_and_b64 vcc, exec, s[0:1]
	s_cbranch_vccnz .LBB2_44
	s_add_u32 s76, s4, 0x40000
	s_addc_u32 s5, s17, 0
	s_and_b32 s77, s5, 0xffff
	s_mov_b32 s78, s6
	s_mov_b32 s79, s7
	s_mov_b32 m0, s44
	s_nop 0
	buffer_load_dwordx4 v193, s[76:79], 0 offen lds
	s_mov_b32 m0, s45
	s_nop 0
	buffer_load_dwordx4 v197, s[76:79], 0 offen lds
.LBB2_44:
	s_waitcnt lgkmcnt(8)
	s_barrier
	s_waitcnt lgkmcnt(0)
	v_mfma_i32_16x16x64_i8 v[124:127], v[128:131], v[184:187], v[124:127]
	v_mfma_i32_16x16x64_i8 v[120:123], v[132:135], v[184:187], v[120:123]
	v_mfma_i32_16x16x64_i8 v[108:111], v[128:131], v[172:175], v[108:111]
	v_mfma_i32_16x16x64_i8 v[104:107], v[132:135], v[172:175], v[104:107]
	v_mfma_i32_16x16x64_i8 v[96:99], v[128:131], v[168:171], v[96:99]
	v_mfma_i32_16x16x64_i8 v[88:91], v[132:135], v[168:171], v[88:91]
	v_mfma_i32_16x16x64_i8 v[80:83], v[128:131], v[160:163], v[80:83]
	v_mfma_i32_16x16x64_i8 v[72:75], v[132:135], v[160:163], v[72:75]
	v_mfma_i32_16x16x64_i8 v[124:127], v[140:143], v[188:191], v[124:127]
	v_mfma_i32_16x16x64_i8 v[120:123], v[136:139], v[188:191], v[120:123]
	v_mfma_i32_16x16x64_i8 v[108:111], v[140:143], v[176:179], v[108:111]
	v_mfma_i32_16x16x64_i8 v[104:107], v[136:139], v[176:179], v[104:107]
	v_mfma_i32_16x16x64_i8 v[96:99], v[140:143], v[180:183], v[96:99]
	v_mfma_i32_16x16x64_i8 v[88:91], v[136:139], v[180:183], v[88:91]
	v_mfma_i32_16x16x64_i8 v[80:83], v[140:143], v[164:167], v[80:83]
	v_mfma_i32_16x16x64_i8 v[72:75], v[136:139], v[164:167], v[72:75]
	s_barrier
	ds_read_b128 v[144:147], v212
	ds_read_b128 v[148:151], v212 offset:2048
	ds_read_b128 v[156:159], v213
	ds_read_b128 v[152:155], v213 offset:2048
	s_and_b64 vcc, exec, s[0:1]
	s_cbranch_vccnz .LBB2_46
	s_add_u32 s76, s16, 0x80
	s_addc_u32 s5, s75, 0
	s_and_b32 s77, s5, 0xffff
	s_mov_b32 s78, s6
	s_mov_b32 s79, s7
	s_mov_b32 m0, s47
	s_nop 0
	buffer_load_dwordx4 v196, s[76:79], 0 offen lds
	s_mov_b32 m0, s48
	s_nop 0
	buffer_load_dwordx4 v198, s[76:79], 0 offen lds
.LBB2_46:
	s_barrier
	s_waitcnt lgkmcnt(0)
	v_mfma_i32_16x16x64_i8 v[116:119], v[144:147], v[184:187], v[116:119]
	v_mfma_i32_16x16x64_i8 v[112:115], v[148:151], v[184:187], v[112:115]
	v_mfma_i32_16x16x64_i8 v[100:103], v[144:147], v[172:175], v[100:103]
	v_mfma_i32_16x16x64_i8 v[92:95], v[148:151], v[172:175], v[92:95]
	v_mfma_i32_16x16x64_i8 v[84:87], v[144:147], v[168:171], v[84:87]
	v_mfma_i32_16x16x64_i8 v[76:79], v[148:151], v[168:171], v[76:79]
	v_mfma_i32_16x16x64_i8 v[68:71], v[144:147], v[160:163], v[68:71]
	v_mfma_i32_16x16x64_i8 v[64:67], v[148:151], v[160:163], v[64:67]
	v_mfma_i32_16x16x64_i8 v[116:119], v[156:159], v[188:191], v[116:119]
	v_mfma_i32_16x16x64_i8 v[112:115], v[152:155], v[188:191], v[112:115]
	v_mfma_i32_16x16x64_i8 v[100:103], v[156:159], v[176:179], v[100:103]
	v_mfma_i32_16x16x64_i8 v[92:95], v[152:155], v[176:179], v[92:95]
	v_mfma_i32_16x16x64_i8 v[84:87], v[156:159], v[180:183], v[84:87]
	v_mfma_i32_16x16x64_i8 v[76:79], v[152:155], v[180:183], v[76:79]
	v_mfma_i32_16x16x64_i8 v[68:71], v[156:159], v[164:167], v[68:71]
	v_mfma_i32_16x16x64_i8 v[64:67], v[152:155], v[164:167], v[64:67]
	s_barrier
	ds_read_b128 v[184:187], v205 offset:49152
	ds_read_b128 v[172:175], v205 offset:51200
	ds_read_b128 v[188:191], v206 offset:49152
	ds_read_b128 v[176:179], v206 offset:51200
	ds_read_b128 v[168:171], v205 offset:53248
	ds_read_b128 v[160:163], v205 offset:55296
	ds_read_b128 v[180:183], v206 offset:53248
	ds_read_b128 v[164:167], v206 offset:55296
	s_and_b64 vcc, exec, s[0:1]
	s_cbranch_vccnz .LBB2_48
	s_add_u32 s4, s4, 0x80
	s_addc_u32 s5, s17, 0
	s_and_b32 s5, s5, 0xffff
	s_mov_b32 m0, s49
	s_nop 0
	buffer_load_dwordx4 v193, s[4:7], 0 offen lds
	s_mov_b32 m0, s50
	s_nop 0
	buffer_load_dwordx4 v197, s[4:7], 0 offen lds
.LBB2_48:
	s_barrier
	s_waitcnt lgkmcnt(0)
	v_mfma_i32_16x16x64_i8 v[60:63], v[128:131], v[184:187], v[60:63]
	v_mfma_i32_16x16x64_i8 v[56:59], v[132:135], v[184:187], v[56:59]
	v_mfma_i32_16x16x64_i8 v[52:55], v[128:131], v[172:175], v[52:55]
	v_mfma_i32_16x16x64_i8 v[44:47], v[132:135], v[172:175], v[44:47]
	v_mfma_i32_16x16x64_i8 v[36:39], v[128:131], v[168:171], v[36:39]
	v_mfma_i32_16x16x64_i8 v[28:31], v[132:135], v[168:171], v[28:31]
	v_mfma_i32_16x16x64_i8 v[20:23], v[128:131], v[160:163], v[20:23]
	v_mfma_i32_16x16x64_i8 v[12:15], v[132:135], v[160:163], v[12:15]
	v_mfma_i32_16x16x64_i8 v[60:63], v[140:143], v[188:191], v[60:63]
	v_mfma_i32_16x16x64_i8 v[56:59], v[136:139], v[188:191], v[56:59]
	v_mfma_i32_16x16x64_i8 v[52:55], v[140:143], v[176:179], v[52:55]
	v_mfma_i32_16x16x64_i8 v[44:47], v[136:139], v[176:179], v[44:47]
	v_mfma_i32_16x16x64_i8 v[36:39], v[140:143], v[180:183], v[36:39]
	v_mfma_i32_16x16x64_i8 v[28:31], v[136:139], v[180:183], v[28:31]
	v_mfma_i32_16x16x64_i8 v[20:23], v[140:143], v[164:167], v[20:23]
	v_mfma_i32_16x16x64_i8 v[12:15], v[136:139], v[164:167], v[12:15]
	s_barrier
	s_and_b64 vcc, exec, s[0:1]
	s_cbranch_vccnz .LBB2_33
	s_add_u32 s4, s16, 0x4080
	s_addc_u32 s0, s75, 0
	s_and_b32 s5, s0, 0xffff
	s_mov_b32 m0, s51
	s_nop 0
	buffer_load_dwordx4 v196, s[4:7], 0 offen lds
	s_mov_b32 m0, s52
	s_nop 0
	buffer_load_dwordx4 v198, s[4:7], 0 offen lds
	s_branch .LBB2_33

.Lp2_sum_skip:
	s_barrier
	buffer_load_dwordx4 v194, s[12:15], 0 offen lds
	s_mov_b32 m0, s41
	v_lshrrev_b32_e32 v2, 4, v0
	buffer_load_dwordx4 v196, s[12:15], 0 offen lds
	s_add_u32 s12, s16, 0x80
	s_addc_u32 s0, s9, 0
	s_add_i32 s42, s31, 0x8000
	s_and_b32 s13, s0, 0xffff
	s_mov_b32 m0, s42
	s_add_i32 s43, s31, 0xa000
	buffer_load_dwordx4 v1, s[12:15], 0 offen lds
	s_mov_b32 m0, s43
	v_and_b32_e32 v197, 15, v0
	buffer_load_dwordx4 v195, s[12:15], 0 offen lds
	s_add_u32 s12, s8, 0x10080
	s_addc_u32 s0, s25, 0
	s_add_i32 s44, s31, 0x1c000
	s_and_b32 s13, s0, 0xffff
	s_mov_b32 m0, s44
	s_add_i32 s45, s31, 0x1e000
	buffer_load_dwordx4 v194, s[12:15], 0 offen lds
	s_mov_b32 m0, s45
	s_and_b32 s0, s2, 1
	buffer_load_dwordx4 v196, s[12:15], 0 offen lds
	s_lshl_b32 s0, s0, 23
	s_lshl_b32 s1, s26, 21
	v_bfe_u32 v3, v0, 1, 3
	s_or_b32 s0, s0, s1
	v_bitop3_b32 v2, v2, v3, 3 bitop3:0x6c
	v_lshlrev_b32_e32 v3, 7, v197
	s_add_i32 s46, s31, 0xc000
	s_add_i32 s47, s31, 0xe000
	s_or_b32 s0, s27, s0
	v_lshlrev_b32_e32 v2, 4, v2
	v_lshl_or_b32 v4, s28, 13, v3
	v_lshl_or_b32 v3, s39, 12, v3
	s_waitcnt vmcnt(6)
	s_add_u32 s48, s20, s0
	v_or_b32_e32 v5, v4, v2
	v_bitop3_b32 v4, v4, 64, v2 bitop3:0x36
	v_or_b32_e32 v198, v3, v2
	v_bitop3_b32 v199, v3, 64, v2 bitop3:0x36
	s_addc_u32 s49, s21, 0
	v_mov_b32_e32 v66, 0
	s_add_i32 s0, 0, 0x10000
	s_add_i32 s1, 0, 0x14000
	s_mov_b32 s50, -2
	s_mov_b64 s[10:11], 0
	v_add_u32_e32 v200, 0, v5
	v_add_u32_e32 v201, 0, v4
	v_mov_b32_e32 v67, v66
	v_mov_b32_e32 v68, v66
	v_mov_b32_e32 v69, v66
	v_mov_b32_e32 v70, v66
	v_mov_b32_e32 v71, v66
	v_mov_b32_e32 v72, v66
	v_mov_b32_e32 v73, v66
	v_mov_b32_e32 v82, v66
	v_mov_b32_e32 v83, v66
	v_mov_b32_e32 v84, v66
	v_mov_b32_e32 v85, v66
	v_mov_b32_e32 v86, v66
	v_mov_b32_e32 v87, v66
	v_mov_b32_e32 v88, v66
	v_mov_b32_e32 v89, v66
	v_mov_b32_e32 v98, v66
	v_mov_b32_e32 v99, v66
	v_mov_b32_e32 v100, v66
	v_mov_b32_e32 v101, v66
	v_mov_b32_e32 v102, v66
	v_mov_b32_e32 v103, v66
	v_mov_b32_e32 v104, v66
	v_mov_b32_e32 v105, v66
	v_mov_b32_e32 v114, v66
	v_mov_b32_e32 v115, v66
	v_mov_b32_e32 v116, v66
	v_mov_b32_e32 v117, v66
	v_mov_b32_e32 v118, v66
	v_mov_b32_e32 v119, v66
	v_mov_b32_e32 v120, v66
	v_mov_b32_e32 v121, v66
	v_mov_b32_e32 v74, v66
	v_mov_b32_e32 v75, v66
	v_mov_b32_e32 v76, v66
	v_mov_b32_e32 v77, v66
	v_mov_b32_e32 v78, v66
	v_mov_b32_e32 v79, v66
	v_mov_b32_e32 v80, v66
	v_mov_b32_e32 v81, v66
	v_mov_b32_e32 v90, v66
	v_mov_b32_e32 v91, v66
	v_mov_b32_e32 v92, v66
	v_mov_b32_e32 v93, v66
	v_mov_b32_e32 v94, v66
	v_mov_b32_e32 v95, v66
	v_mov_b32_e32 v96, v66
	v_mov_b32_e32 v97, v66
	v_mov_b32_e32 v106, v66
	v_mov_b32_e32 v107, v66
	v_mov_b32_e32 v108, v66
	v_mov_b32_e32 v109, v66
	v_mov_b32_e32 v110, v66
	v_mov_b32_e32 v111, v66
	v_mov_b32_e32 v112, v66
	v_mov_b32_e32 v113, v66
	v_mov_b32_e32 v122, v66
	v_mov_b32_e32 v123, v66
	v_mov_b32_e32 v124, v66
	v_mov_b32_e32 v125, v66
	v_mov_b32_e32 v126, v66
	v_mov_b32_e32 v127, v66
	v_mov_b32_e32 v128, v66
	v_mov_b32_e32 v129, v66
	v_mov_b32_e32 v130, v66
	v_mov_b32_e32 v131, v66
	v_mov_b32_e32 v132, v66
	v_mov_b32_e32 v133, v66
	v_mov_b32_e32 v134, v66
	v_mov_b32_e32 v135, v66
	v_mov_b32_e32 v136, v66
	v_mov_b32_e32 v137, v66
	v_mov_b32_e32 v146, v66
	v_mov_b32_e32 v147, v66
	v_mov_b32_e32 v148, v66
	v_mov_b32_e32 v149, v66
	v_mov_b32_e32 v150, v66
	v_mov_b32_e32 v151, v66
	v_mov_b32_e32 v152, v66
	v_mov_b32_e32 v153, v66
	v_mov_b32_e32 v162, v66
	v_mov_b32_e32 v163, v66
	v_mov_b32_e32 v164, v66
	v_mov_b32_e32 v165, v66
	v_mov_b32_e32 v166, v66
	v_mov_b32_e32 v167, v66
	v_mov_b32_e32 v168, v66
	v_mov_b32_e32 v169, v66
	v_mov_b32_e32 v178, v66
	v_mov_b32_e32 v179, v66
	v_mov_b32_e32 v180, v66
	v_mov_b32_e32 v181, v66
	v_mov_b32_e32 v182, v66
	v_mov_b32_e32 v183, v66
	v_mov_b32_e32 v184, v66
	v_mov_b32_e32 v185, v66
	v_mov_b32_e32 v138, v66
	v_mov_b32_e32 v139, v66
	v_mov_b32_e32 v140, v66
	v_mov_b32_e32 v141, v66
	v_mov_b32_e32 v142, v66
	v_mov_b32_e32 v143, v66
	v_mov_b32_e32 v144, v66
	v_mov_b32_e32 v145, v66
	v_mov_b32_e32 v154, v66
	v_mov_b32_e32 v155, v66
	v_mov_b32_e32 v156, v66
	v_mov_b32_e32 v157, v66
	v_mov_b32_e32 v158, v66
	v_mov_b32_e32 v159, v66
	v_mov_b32_e32 v160, v66
	v_mov_b32_e32 v161, v66
	v_mov_b32_e32 v170, v66
	v_mov_b32_e32 v171, v66
	v_mov_b32_e32 v172, v66
	v_mov_b32_e32 v173, v66
	v_mov_b32_e32 v174, v66
	v_mov_b32_e32 v175, v66
	v_mov_b32_e32 v176, v66
	v_mov_b32_e32 v177, v66
	v_mov_b32_e32 v186, v66
	v_mov_b32_e32 v187, v66
	v_mov_b32_e32 v188, v66
	v_mov_b32_e32 v189, v66
	v_mov_b32_e32 v190, v66
	v_mov_b32_e32 v191, v66
	v_mov_b32_e32 v192, v66
	v_mov_b32_e32 v193, v66
	v_bfe_u32 v202, v0, 4, 2
	v_add_u32_e32 v203, s0, v198
	v_add_u32_e32 v204, s0, v199
	v_add_u32_e32 v205, s1, v198
	v_add_u32_e32 v206, s1, v199
	s_barrier
	s_cmpk_eq_i32 s10, 0x700
	s_cselect_b64 s[18:19], -1, 0
	s_cmpk_lg_i32 s10, 0x700
	s_cselect_b64 s[26:27], -1, 0
	s_add_u32 s54, s48, s10
	s_addc_u32 s55, s49, s11
	s_add_u32 s51, s8, s10
	s_addc_u32 s52, s25, s11
	s_add_u32 s20, s51, 0x100
	s_addc_u32 s53, s52, 0
	s_add_u32 s12, s54, 0x100080
	s_addc_u32 s0, s55, 0
	s_and_b32 s13, s0, 0xffff
	v_add_u32_e32 v210, 0x1c000, v198
	v_add_u32_e32 v211, 0x1c000, v199
	s_cmpk_lt_u32 s3, 0x100
	s_cbranch_scc1 .Lp2_prio_done
	s_setprio 1

.LBB3_3:
	s_waitcnt vmcnt(10)
	s_barrier
	v_mfma_f32_16x16x128_f8f6f4 v[118:121], v[26:33], v[58:65], v[118:121]
	s_add_i32 s50, s50, 2
	s_add_u32 s10, s10, 0x100
	s_addc_u32 s11, s11, 0
	v_mfma_f32_16x16x128_f8f6f4 v[114:117], v[18:25], v[58:65], v[114:117]
	s_cmpk_eq_i32 s10, 0x700
	s_cselect_b64 s[18:19], -1, 0
	s_cmpk_lg_i32 s10, 0x700
	s_cselect_b64 s[26:27], -1, 0
	v_mfma_f32_16x16x128_f8f6f4 v[102:105], v[26:33], v[50:57], v[102:105]
	s_add_u32 s54, s48, s10
	s_addc_u32 s55, s49, s11
	s_add_u32 s51, s8, s10
	s_addc_u32 s52, s25, s11
	v_mfma_f32_16x16x128_f8f6f4 v[98:101], v[18:25], v[50:57], v[98:101]
	s_add_u32 s20, s51, 0x100
	s_addc_u32 s53, s52, 0
	s_add_u32 s12, s54, 0x100080
	s_addc_u32 s0, s55, 0
	v_mfma_f32_16x16x128_f8f6f4 v[86:89], v[26:33], v[42:49], v[86:89]
	s_and_b32 s13, s0, 0xffff
	s_cmp_gt_u32 s50, 13
	v_mfma_f32_16x16x128_f8f6f4 v[82:85], v[18:25], v[42:49], v[82:85]
	v_mfma_f32_16x16x128_f8f6f4 v[70:73], v[26:33], v[34:41], v[70:73]
	v_mfma_f32_16x16x128_f8f6f4 v[66:69], v[18:25], v[34:41], v[66:69]
	s_barrier
	s_cbranch_scc1 .LBB3_20
.LBB3_4:
	ds_read_b128 v[2:5], v203
	ds_read_b128 v[10:13], v203 offset:2048
	ds_read_b128 v[6:9], v204
	ds_read_b128 v[14:17], v204 offset:2048
	s_mov_b32 m0, s46
	ds_read_b128 v[58:61], v200
	ds_read_b128 v[50:53], v200 offset:2048
	ds_read_b128 v[62:65], v201
	ds_read_b128 v[54:57], v201 offset:2048
	ds_read_b128 v[42:45], v200 offset:4096
	ds_read_b128 v[34:37], v200 offset:6144
	ds_read_b128 v[46:49], v201 offset:4096
	ds_read_b128 v[38:41], v201 offset:6144
	s_waitcnt vmcnt(8)
	buffer_load_dwordx4 v1, s[12:15], 0 offen lds
	s_mov_b32 m0, s47
	s_nop 0
	buffer_load_dwordx4 v195, s[12:15], 0 offen lds
	s_waitcnt lgkmcnt(8)
	s_barrier
	s_waitcnt lgkmcnt(0)
	v_mfma_f32_16x16x128_f8f6f4 v[190:193], v[2:9], v[58:65], v[190:193]
	v_mfma_f32_16x16x128_f8f6f4 v[186:189], v[10:17], v[58:65], v[186:189]
	v_mfma_f32_16x16x128_f8f6f4 v[174:177], v[2:9], v[50:57], v[174:177]
	v_mfma_f32_16x16x128_f8f6f4 v[170:173], v[10:17], v[50:57], v[170:173]
	v_mfma_f32_16x16x128_f8f6f4 v[158:161], v[2:9], v[42:49], v[158:161]
	v_mfma_f32_16x16x128_f8f6f4 v[154:157], v[10:17], v[42:49], v[154:157]
	v_mfma_f32_16x16x128_f8f6f4 v[142:145], v[2:9], v[34:41], v[142:145]
	v_mfma_f32_16x16x128_f8f6f4 v[138:141], v[10:17], v[34:41], v[138:141]
	s_barrier
	ds_read_b128 v[26:29], v205
	ds_read_b128 v[18:21], v205 offset:2048
	ds_read_b128 v[30:33], v206
	ds_read_b128 v[22:25], v206 offset:2048
	s_waitcnt vmcnt(8)
	s_and_b64 vcc, exec, s[18:19]
	s_cbranch_vccnz .LBB3_6
	s_and_b32 s21, s53, 0xffff
	s_mov_b32 s22, s14
	s_mov_b32 s23, s15
	s_mov_b32 m0, s33
	s_nop 0
	buffer_load_dwordx4 v194, s[20:23], 0 offen lds
	s_mov_b32 m0, s34
	s_nop 0
	buffer_load_dwordx4 v196, s[20:23], 0 offen lds
.LBB3_6:
	s_barrier
	s_waitcnt lgkmcnt(0)
	v_mfma_f32_16x16x128_f8f6f4 v[182:185], v[26:33], v[58:65], v[182:185]
	s_add_u32 s12, s54, 0x100
	s_addc_u32 s21, s55, 0
	v_mfma_f32_16x16x128_f8f6f4 v[178:181], v[18:25], v[58:65], v[178:181]
	v_mfma_f32_16x16x128_f8f6f4 v[166:169], v[26:33], v[50:57], v[166:169]
	v_mfma_f32_16x16x128_f8f6f4 v[162:165], v[18:25], v[50:57], v[162:165]
	v_mfma_f32_16x16x128_f8f6f4 v[150:153], v[26:33], v[42:49], v[150:153]
	v_mfma_f32_16x16x128_f8f6f4 v[146:149], v[18:25], v[42:49], v[146:149]
	v_mfma_f32_16x16x128_f8f6f4 v[134:137], v[26:33], v[34:41], v[134:137]
	v_mfma_f32_16x16x128_f8f6f4 v[130:133], v[18:25], v[34:41], v[130:133]
	s_barrier
	ds_read_b128 v[58:61], v200 offset:16384
	ds_read_b128 v[50:53], v200 offset:18432
	ds_read_b128 v[62:65], v201 offset:16384
	ds_read_b128 v[54:57], v201 offset:18432
	ds_read_b128 v[42:45], v200 offset:20480
	ds_read_b128 v[34:37], v200 offset:22528
	ds_read_b128 v[46:49], v201 offset:20480
	ds_read_b128 v[38:41], v201 offset:22528
	v_cndmask_b32_e64 v207, 0, 1, s[26:27]
	v_cmp_ne_u32_e64 s[0:1], 1, v207
	s_andn2_b64 vcc, exec, s[26:27]
	s_cbranch_vccnz .LBB3_8
	s_and_b32 s13, s21, 0xffff
	s_mov_b32 m0, s31
	s_nop 0
	buffer_load_dwordx4 v1, s[12:15], 0 offen lds
	s_mov_b32 m0, s35
	s_nop 0
	buffer_load_dwordx4 v195, s[12:15], 0 offen lds
.LBB3_8:
	s_barrier
	s_waitcnt lgkmcnt(0)
	v_mfma_f32_16x16x128_f8f6f4 v[126:129], v[2:9], v[58:65], v[126:129]
	v_mfma_f32_16x16x128_f8f6f4 v[122:125], v[10:17], v[58:65], v[122:125]
	v_mfma_f32_16x16x128_f8f6f4 v[110:113], v[2:9], v[50:57], v[110:113]
	v_mfma_f32_16x16x128_f8f6f4 v[106:109], v[10:17], v[50:57], v[106:109]
	v_mfma_f32_16x16x128_f8f6f4 v[94:97], v[2:9], v[42:49], v[94:97]
	v_mfma_f32_16x16x128_f8f6f4 v[90:93], v[10:17], v[42:49], v[90:93]
	v_mfma_f32_16x16x128_f8f6f4 v[78:81], v[2:9], v[34:41], v[78:81]
	v_mfma_f32_16x16x128_f8f6f4 v[74:77], v[10:17], v[34:41], v[74:77]
	s_barrier
	s_and_b64 vcc, exec, s[0:1]
	s_mov_b64 s[22:23], -1
	s_cbranch_vccnz .LBB3_10
	s_add_u32 s56, s51, 0x10100
	s_addc_u32 s13, s52, 0
	s_mov_b32 m0, s17
	s_and_b32 s57, s13, 0xffff
	s_mov_b32 s58, s14
	s_mov_b32 s59, s15
	buffer_load_dwordx4 v194, s[56:59], 0 offen lds
	s_mov_b32 m0, s36
	s_mov_b64 s[22:23], 0
	buffer_load_dwordx4 v196, s[56:59], 0 offen lds
	s_waitcnt vmcnt(10)

.LBB3_12:
	s_barrier
	v_mfma_f32_16x16x128_f8f6f4 v[118:121], v[26:33], v[58:65], v[118:121]
	s_add_i32 s13, 0, 0x18000
	v_add_u32_e32 v2, s13, v198
	v_add_u32_e32 v6, s13, v199
	v_mfma_f32_16x16x128_f8f6f4 v[114:117], v[18:25], v[58:65], v[114:117]
	v_mfma_f32_16x16x128_f8f6f4 v[102:105], v[26:33], v[50:57], v[102:105]
	v_mfma_f32_16x16x128_f8f6f4 v[98:101], v[18:25], v[50:57], v[98:101]
	v_mfma_f32_16x16x128_f8f6f4 v[86:89], v[26:33], v[42:49], v[86:89]
	v_mfma_f32_16x16x128_f8f6f4 v[82:85], v[18:25], v[42:49], v[82:85]
	v_mfma_f32_16x16x128_f8f6f4 v[70:73], v[26:33], v[34:41], v[70:73]
	v_mfma_f32_16x16x128_f8f6f4 v[66:69], v[18:25], v[34:41], v[66:69]
	s_barrier
	ds_read_b128 v[10:13], v2
	ds_read_b128 v[2:5], v2 offset:2048
	ds_read_b128 v[14:17], v6
	ds_read_b128 v[6:9], v6 offset:2048
	ds_read_b128 v[58:61], v200 offset:32768
	ds_read_b128 v[50:53], v200 offset:34816
	ds_read_b128 v[62:65], v201 offset:32768
	ds_read_b128 v[54:57], v201 offset:34816
	ds_read_b128 v[42:45], v200 offset:36864
	ds_read_b128 v[34:37], v200 offset:38912
	ds_read_b128 v[46:49], v201 offset:36864
	ds_read_b128 v[38:41], v201 offset:38912
	s_waitcnt vmcnt(8)
	s_and_b64 vcc, exec, s[0:1]
	s_cbranch_vccnz .LBB3_14
	s_add_u32 s56, s54, 0x100100
	s_addc_u32 s13, s55, 0
	s_and_b32 s57, s13, 0xffff
	s_mov_b32 s58, s14
	s_mov_b32 s59, s15
	s_mov_b32 m0, s37
	s_nop 0
	buffer_load_dwordx4 v1, s[56:59], 0 offen lds
	s_mov_b32 m0, s38
	s_nop 0
	buffer_load_dwordx4 v195, s[56:59], 0 offen lds
.LBB3_14:
	s_waitcnt lgkmcnt(8)
	s_barrier
	s_waitcnt lgkmcnt(0)
	v_mfma_f32_16x16x128_f8f6f4 v[190:193], v[10:17], v[58:65], v[190:193]
	v_mfma_f32_16x16x128_f8f6f4 v[186:189], v[2:9], v[58:65], v[186:189]
	v_mfma_f32_16x16x128_f8f6f4 v[174:177], v[10:17], v[50:57], v[174:177]
	v_mfma_f32_16x16x128_f8f6f4 v[170:173], v[2:9], v[50:57], v[170:173]
	v_mfma_f32_16x16x128_f8f6f4 v[158:161], v[10:17], v[42:49], v[158:161]
	v_mfma_f32_16x16x128_f8f6f4 v[154:157], v[2:9], v[42:49], v[154:157]
	v_mfma_f32_16x16x128_f8f6f4 v[142:145], v[10:17], v[34:41], v[142:145]
	v_mfma_f32_16x16x128_f8f6f4 v[138:141], v[2:9], v[34:41], v[138:141]
	s_barrier
	ds_read_b128 v[26:29], v210
	ds_read_b128 v[18:21], v210 offset:2048
	ds_read_b128 v[30:33], v211
	ds_read_b128 v[22:25], v211 offset:2048
	s_waitcnt vmcnt(8)
	s_and_b64 vcc, exec, s[0:1]
	s_cbranch_vccnz .LBB3_16
	s_and_b64 s[22:23], exec, s[18:19]
	s_cselect_b32 s20, s8, s20
	s_cselect_b32 s13, s25, s53
	s_add_u32 s56, s20, 0x80
	s_addc_u32 s13, s13, 0
	s_and_b32 s57, s13, 0xffff
	s_mov_b32 s58, s14
	s_mov_b32 s59, s15
	s_mov_b32 m0, s40
	s_nop 0
	buffer_load_dwordx4 v194, s[56:59], 0 offen lds
	s_mov_b32 m0, s41
	s_nop 0
	buffer_load_dwordx4 v196, s[56:59], 0 offen lds
.LBB3_16:
	s_barrier
	s_waitcnt lgkmcnt(0)
	v_mfma_f32_16x16x128_f8f6f4 v[182:185], v[26:33], v[58:65], v[182:185]
	v_mfma_f32_16x16x128_f8f6f4 v[178:181], v[18:25], v[58:65], v[178:181]
	v_mfma_f32_16x16x128_f8f6f4 v[166:169], v[26:33], v[50:57], v[166:169]
	v_mfma_f32_16x16x128_f8f6f4 v[162:165], v[18:25], v[50:57], v[162:165]
	v_mfma_f32_16x16x128_f8f6f4 v[150:153], v[26:33], v[42:49], v[150:153]
	v_mfma_f32_16x16x128_f8f6f4 v[146:149], v[18:25], v[42:49], v[146:149]
	v_mfma_f32_16x16x128_f8f6f4 v[134:137], v[26:33], v[34:41], v[134:137]
	v_mfma_f32_16x16x128_f8f6f4 v[130:133], v[18:25], v[34:41], v[130:133]
	s_barrier
	ds_read_b128 v[58:61], v200 offset:49152
	ds_read_b128 v[50:53], v200 offset:51200
	ds_read_b128 v[62:65], v201 offset:49152
	ds_read_b128 v[54:57], v201 offset:51200
	ds_read_b128 v[42:45], v200 offset:53248
	ds_read_b128 v[34:37], v200 offset:55296
	ds_read_b128 v[46:49], v201 offset:53248
	ds_read_b128 v[38:41], v201 offset:55296
	s_and_b64 vcc, exec, s[0:1]
	s_cbranch_vccnz .LBB3_18
	s_and_b64 s[18:19], exec, s[18:19]
	s_cselect_b32 s12, s16, s12
	s_cselect_b32 s13, s9, s21
	s_add_u32 s12, s12, 0x80
	s_addc_u32 s13, s13, 0
	s_and_b32 s13, s13, 0xffff
	s_mov_b32 m0, s42
	s_nop 0
	buffer_load_dwordx4 v1, s[12:15], 0 offen lds
	s_mov_b32 m0, s43
	s_nop 0
	buffer_load_dwordx4 v195, s[12:15], 0 offen lds
.LBB3_18:
	s_barrier
	s_waitcnt lgkmcnt(0)
	v_mfma_f32_16x16x128_f8f6f4 v[126:129], v[10:17], v[58:65], v[126:129]
	v_mfma_f32_16x16x128_f8f6f4 v[122:125], v[2:9], v[58:65], v[122:125]
	v_mfma_f32_16x16x128_f8f6f4 v[110:113], v[10:17], v[50:57], v[110:113]
	v_mfma_f32_16x16x128_f8f6f4 v[106:109], v[2:9], v[50:57], v[106:109]
	v_mfma_f32_16x16x128_f8f6f4 v[94:97], v[10:17], v[42:49], v[94:97]
	v_mfma_f32_16x16x128_f8f6f4 v[90:93], v[2:9], v[42:49], v[90:93]
	v_mfma_f32_16x16x128_f8f6f4 v[78:81], v[10:17], v[34:41], v[78:81]
	v_mfma_f32_16x16x128_f8f6f4 v[74:77], v[2:9], v[34:41], v[74:77]
	s_barrier
	s_and_b64 vcc, exec, s[0:1]
	s_cbranch_vccnz .LBB3_3
	s_add_u32 s12, s51, 0x10180
	s_addc_u32 s0, s52, 0
	s_and_b32 s13, s0, 0xffff
	s_mov_b32 m0, s44
	s_nop 0
	buffer_load_dwordx4 v194, s[12:15], 0 offen lds
	s_mov_b32 m0, s45
	s_nop 0
	buffer_load_dwordx4 v196, s[12:15], 0 offen lds
	s_branch .LBB3_3

.LBB4_12:
	s_and_b32 s33, s0, 3
	s_add_u32 s12, s8, 0x80
	s_addc_u32 s0, s3, 0
	s_add_i32 s36, s7, 0x18000
	s_and_b32 s13, s0, 0xffff
	s_mov_b32 m0, s36
	s_add_i32 s37, s7, 0x1a000
	s_waitcnt vmcnt(4)
	s_barrier
	buffer_load_dwordx4 v193, s[12:15], 0 offen lds
	s_mov_b32 m0, s37
	v_lshrrev_b32_e32 v1, 4, v0
	buffer_load_dwordx4 v195, s[12:15], 0 offen lds
	s_add_u32 s12, s16, 0x80
	s_addc_u32 s0, s9, 0
	s_add_i32 s38, s7, 0x8000
	s_and_b32 s13, s0, 0xffff
	s_mov_b32 m0, s38
	s_add_i32 s39, s7, 0xa000
	buffer_load_dwordx4 v192, s[12:15], 0 offen lds
	s_mov_b32 m0, s39
	v_and_b32_e32 v196, 15, v0
	buffer_load_dwordx4 v194, s[12:15], 0 offen lds
	s_add_u32 s12, s8, 0x4080
	s_addc_u32 s0, s3, 0
	s_add_i32 s40, s7, 0x1c000
	s_and_b32 s13, s0, 0xffff
	s_mov_b32 m0, s40
	s_add_i32 s41, s7, 0x1e000
	buffer_load_dwordx4 v193, s[12:15], 0 offen lds
	s_mov_b32 m0, s41
	v_bfe_u32 v197, v0, 4, 2
	buffer_load_dwordx4 v195, s[12:15], 0 offen lds
	v_bfe_u32 v0, v0, 1, 3
	v_bitop3_b32 v0, v1, v0, 3 bitop3:0x6c
	v_lshlrev_b32_e32 v1, 7, v196
	v_lshlrev_b32_e32 v0, 4, v0
	v_lshl_or_b32 v2, s27, 13, v1
	v_lshl_or_b32 v1, s33, 12, v1
	s_waitcnt vmcnt(6)
	v_or_b32_e32 v3, v2, v0
	v_or_b32_e32 v198, v1, v0
	v_bitop3_b32 v2, v2, 64, v0 bitop3:0x36
	v_bitop3_b32 v199, v1, 64, v0 bitop3:0x36
	v_mov_b32_e32 v64, 0
	s_add_i32 s0, 0, 0x10000
	s_add_i32 s1, 0, 0x14000
	s_add_i32 s42, s7, 0xc000
	s_add_i32 s43, s7, 0xe000
	s_mov_b32 s44, -2
	s_mov_b64 s[10:11], 0
	v_add_u32_e32 v200, 0, v3
	v_add_u32_e32 v201, 0, v2
	s_add_i32 s45, 0, 0x18000
	v_mov_b32_e32 v65, v64
	v_mov_b32_e32 v66, v64
	v_mov_b32_e32 v67, v64
	v_mov_b32_e32 v68, v64
	v_mov_b32_e32 v69, v64
	v_mov_b32_e32 v70, v64
	v_mov_b32_e32 v71, v64
	v_mov_b32_e32 v80, v64
	v_mov_b32_e32 v81, v64
	v_mov_b32_e32 v82, v64
	v_mov_b32_e32 v83, v64
	v_mov_b32_e32 v84, v64
	v_mov_b32_e32 v85, v64
	v_mov_b32_e32 v86, v64
	v_mov_b32_e32 v87, v64
	v_mov_b32_e32 v96, v64
	v_mov_b32_e32 v97, v64
	v_mov_b32_e32 v98, v64
	v_mov_b32_e32 v99, v64
	v_mov_b32_e32 v100, v64
	v_mov_b32_e32 v101, v64
	v_mov_b32_e32 v102, v64
	v_mov_b32_e32 v103, v64
	v_mov_b32_e32 v112, v64
	v_mov_b32_e32 v113, v64
	v_mov_b32_e32 v114, v64
	v_mov_b32_e32 v115, v64
	v_mov_b32_e32 v116, v64
	v_mov_b32_e32 v117, v64
	v_mov_b32_e32 v118, v64
	v_mov_b32_e32 v119, v64
	v_mov_b32_e32 v72, v64
	v_mov_b32_e32 v73, v64
	v_mov_b32_e32 v74, v64
	v_mov_b32_e32 v75, v64
	v_mov_b32_e32 v76, v64
	v_mov_b32_e32 v77, v64
	v_mov_b32_e32 v78, v64
	v_mov_b32_e32 v79, v64
	v_mov_b32_e32 v88, v64
	v_mov_b32_e32 v89, v64
	v_mov_b32_e32 v90, v64
	v_mov_b32_e32 v91, v64
	v_mov_b32_e32 v92, v64
	v_mov_b32_e32 v93, v64
	v_mov_b32_e32 v94, v64
	v_mov_b32_e32 v95, v64
	v_mov_b32_e32 v104, v64
	v_mov_b32_e32 v105, v64
	v_mov_b32_e32 v106, v64
	v_mov_b32_e32 v107, v64
	v_mov_b32_e32 v108, v64
	v_mov_b32_e32 v109, v64
	v_mov_b32_e32 v110, v64
	v_mov_b32_e32 v111, v64
	v_mov_b32_e32 v120, v64
	v_mov_b32_e32 v121, v64
	v_mov_b32_e32 v122, v64
	v_mov_b32_e32 v123, v64
	v_mov_b32_e32 v124, v64
	v_mov_b32_e32 v125, v64
	v_mov_b32_e32 v126, v64
	v_mov_b32_e32 v127, v64
	v_mov_b32_e32 v128, v64
	v_mov_b32_e32 v129, v64
	v_mov_b32_e32 v130, v64
	v_mov_b32_e32 v131, v64
	v_mov_b32_e32 v132, v64
	v_mov_b32_e32 v133, v64
	v_mov_b32_e32 v134, v64
	v_mov_b32_e32 v135, v64
	v_mov_b32_e32 v144, v64
	v_mov_b32_e32 v145, v64
	v_mov_b32_e32 v146, v64
	v_mov_b32_e32 v147, v64
	v_mov_b32_e32 v148, v64
	v_mov_b32_e32 v149, v64
	v_mov_b32_e32 v150, v64
	v_mov_b32_e32 v151, v64
	v_mov_b32_e32 v160, v64
	v_mov_b32_e32 v161, v64
	v_mov_b32_e32 v162, v64
	v_mov_b32_e32 v163, v64
	v_mov_b32_e32 v164, v64
	v_mov_b32_e32 v165, v64
	v_mov_b32_e32 v166, v64
	v_mov_b32_e32 v167, v64
	v_mov_b32_e32 v176, v64
	v_mov_b32_e32 v177, v64
	v_mov_b32_e32 v178, v64
	v_mov_b32_e32 v179, v64
	v_mov_b32_e32 v180, v64
	v_mov_b32_e32 v181, v64
	v_mov_b32_e32 v182, v64
	v_mov_b32_e32 v183, v64
	v_mov_b32_e32 v136, v64
	v_mov_b32_e32 v137, v64
	v_mov_b32_e32 v138, v64
	v_mov_b32_e32 v139, v64
	v_mov_b32_e32 v140, v64
	v_mov_b32_e32 v141, v64
	v_mov_b32_e32 v142, v64
	v_mov_b32_e32 v143, v64
	v_mov_b32_e32 v152, v64
	v_mov_b32_e32 v153, v64
	v_mov_b32_e32 v154, v64
	v_mov_b32_e32 v155, v64
	v_mov_b32_e32 v156, v64
	v_mov_b32_e32 v157, v64
	v_mov_b32_e32 v158, v64
	v_mov_b32_e32 v159, v64
	v_mov_b32_e32 v168, v64
	v_mov_b32_e32 v169, v64
	v_mov_b32_e32 v170, v64
	v_mov_b32_e32 v171, v64
	v_mov_b32_e32 v172, v64
	v_mov_b32_e32 v173, v64
	v_mov_b32_e32 v174, v64
	v_mov_b32_e32 v175, v64
	v_mov_b32_e32 v184, v64
	v_mov_b32_e32 v185, v64
	v_mov_b32_e32 v186, v64
	v_mov_b32_e32 v187, v64
	v_mov_b32_e32 v188, v64
	v_mov_b32_e32 v189, v64
	v_mov_b32_e32 v190, v64
	v_mov_b32_e32 v191, v64
	v_add_u32_e32 v202, s0, v198
	v_add_u32_e32 v203, s0, v199
	v_add_u32_e32 v204, s1, v198
	v_add_u32_e32 v205, s1, v199
	s_barrier
	s_cmpk_eq_i32 s10, 0x700
	s_cselect_b64 s[18:19], -1, 0
	s_cmpk_lg_i32 s10, 0x700
	s_cselect_b64 s[24:25], -1, 0
	s_add_u32 s49, s16, s10
	s_addc_u32 s50, s9, s11
	s_add_u32 s46, s8, s10
	s_addc_u32 s47, s3, s11
	s_add_u32 s20, s46, 0x100
	s_addc_u32 s48, s47, 0
	s_add_u32 s12, s49, 0x40080
	s_addc_u32 s0, s50, 0
	s_and_b32 s13, s0, 0xffff
	v_add_u32_e32 v207, 0x1c000, v198
	v_add_u32_e32 v208, 0x1c000, v199
	s_cmpk_lt_u32 s26, 0x100
	s_cbranch_scc1 .Lp3_prio_done
	s_setprio 1

.LBB4_13:
	s_waitcnt vmcnt(10)
	s_barrier
	v_mfma_f32_16x16x128_f8f6f4 v[116:119], v[24:31], v[56:63], v[116:119]
	s_add_i32 s44, s44, 2
	s_add_u32 s10, s10, 0x100
	s_addc_u32 s11, s11, 0
	v_mfma_f32_16x16x128_f8f6f4 v[112:115], v[16:23], v[56:63], v[112:115]
	s_cmpk_eq_i32 s10, 0x700
	s_cselect_b64 s[18:19], -1, 0
	s_cmpk_lg_i32 s10, 0x700
	s_cselect_b64 s[24:25], -1, 0
	v_mfma_f32_16x16x128_f8f6f4 v[100:103], v[24:31], v[48:55], v[100:103]
	s_add_u32 s49, s16, s10
	s_addc_u32 s50, s9, s11
	s_add_u32 s46, s8, s10
	s_addc_u32 s47, s3, s11
	v_mfma_f32_16x16x128_f8f6f4 v[96:99], v[16:23], v[48:55], v[96:99]
	s_add_u32 s20, s46, 0x100
	s_addc_u32 s48, s47, 0
	s_add_u32 s12, s49, 0x40080
	s_addc_u32 s0, s50, 0
	v_mfma_f32_16x16x128_f8f6f4 v[84:87], v[24:31], v[40:47], v[84:87]
	s_and_b32 s13, s0, 0xffff
	s_cmp_gt_u32 s44, 13
	v_mfma_f32_16x16x128_f8f6f4 v[80:83], v[16:23], v[40:47], v[80:83]
	v_mfma_f32_16x16x128_f8f6f4 v[68:71], v[24:31], v[32:39], v[68:71]
	v_mfma_f32_16x16x128_f8f6f4 v[64:67], v[16:23], v[32:39], v[64:67]
	s_barrier
	s_cbranch_scc1 .LBB4_30
.LBB4_14:
	ds_read_b128 v[0:3], v202
	ds_read_b128 v[8:11], v202 offset:2048
	ds_read_b128 v[4:7], v203
	ds_read_b128 v[12:15], v203 offset:2048
	s_mov_b32 m0, s42
	ds_read_b128 v[56:59], v200
	ds_read_b128 v[48:51], v200 offset:2048
	ds_read_b128 v[60:63], v201
	ds_read_b128 v[52:55], v201 offset:2048
	ds_read_b128 v[40:43], v200 offset:4096
	ds_read_b128 v[32:35], v200 offset:6144
	ds_read_b128 v[44:47], v201 offset:4096
	ds_read_b128 v[36:39], v201 offset:6144
	s_waitcnt vmcnt(8)
	buffer_load_dwordx4 v192, s[12:15], 0 offen lds
	s_mov_b32 m0, s43
	s_nop 0
	buffer_load_dwordx4 v194, s[12:15], 0 offen lds
	s_waitcnt lgkmcnt(8)
	s_barrier
	s_waitcnt lgkmcnt(0)
	v_mfma_f32_16x16x128_f8f6f4 v[188:191], v[0:7], v[56:63], v[188:191]
	v_mfma_f32_16x16x128_f8f6f4 v[184:187], v[8:15], v[56:63], v[184:187]
	v_mfma_f32_16x16x128_f8f6f4 v[172:175], v[0:7], v[48:55], v[172:175]
	v_mfma_f32_16x16x128_f8f6f4 v[168:171], v[8:15], v[48:55], v[168:171]
	v_mfma_f32_16x16x128_f8f6f4 v[156:159], v[0:7], v[40:47], v[156:159]
	v_mfma_f32_16x16x128_f8f6f4 v[152:155], v[8:15], v[40:47], v[152:155]
	v_mfma_f32_16x16x128_f8f6f4 v[140:143], v[0:7], v[32:39], v[140:143]
	v_mfma_f32_16x16x128_f8f6f4 v[136:139], v[8:15], v[32:39], v[136:139]
	s_barrier
	ds_read_b128 v[24:27], v204
	ds_read_b128 v[16:19], v204 offset:2048
	ds_read_b128 v[28:31], v205
	ds_read_b128 v[20:23], v205 offset:2048
	s_waitcnt vmcnt(8)
	s_and_b64 vcc, exec, s[18:19]
	s_cbranch_vccnz .LBB4_16
	s_and_b32 s21, s48, 0xffff
	s_mov_b32 s22, s14
	s_mov_b32 s23, s15
	s_mov_b32 m0, s28
	s_nop 0
	buffer_load_dwordx4 v193, s[20:23], 0 offen lds
	s_mov_b32 m0, s29
	s_nop 0
	buffer_load_dwordx4 v195, s[20:23], 0 offen lds
.LBB4_16:
	s_barrier
	s_waitcnt lgkmcnt(0)
	v_mfma_f32_16x16x128_f8f6f4 v[180:183], v[24:31], v[56:63], v[180:183]
	s_add_u32 s12, s49, 0x100
	s_addc_u32 s21, s50, 0
	v_mfma_f32_16x16x128_f8f6f4 v[176:179], v[16:23], v[56:63], v[176:179]
	v_mfma_f32_16x16x128_f8f6f4 v[164:167], v[24:31], v[48:55], v[164:167]
	v_mfma_f32_16x16x128_f8f6f4 v[160:163], v[16:23], v[48:55], v[160:163]
	v_mfma_f32_16x16x128_f8f6f4 v[148:151], v[24:31], v[40:47], v[148:151]
	v_mfma_f32_16x16x128_f8f6f4 v[144:147], v[16:23], v[40:47], v[144:147]
	v_mfma_f32_16x16x128_f8f6f4 v[132:135], v[24:31], v[32:39], v[132:135]
	v_mfma_f32_16x16x128_f8f6f4 v[128:131], v[16:23], v[32:39], v[128:131]
	s_barrier
	ds_read_b128 v[56:59], v200 offset:16384
	ds_read_b128 v[48:51], v200 offset:18432
	ds_read_b128 v[60:63], v201 offset:16384
	ds_read_b128 v[52:55], v201 offset:18432
	ds_read_b128 v[40:43], v200 offset:20480
	ds_read_b128 v[32:35], v200 offset:22528
	ds_read_b128 v[44:47], v201 offset:20480
	ds_read_b128 v[36:39], v201 offset:22528
	v_cndmask_b32_e64 v206, 0, 1, s[24:25]
	v_cmp_ne_u32_e64 s[0:1], 1, v206
	s_andn2_b64 vcc, exec, s[24:25]
	s_cbranch_vccnz .LBB4_18
	s_and_b32 s13, s21, 0xffff
	s_mov_b32 m0, s7
	s_nop 0
	buffer_load_dwordx4 v192, s[12:15], 0 offen lds
	s_mov_b32 m0, s30
	s_nop 0
	buffer_load_dwordx4 v194, s[12:15], 0 offen lds
.LBB4_18:
	s_barrier
	s_waitcnt lgkmcnt(0)
	v_mfma_f32_16x16x128_f8f6f4 v[124:127], v[0:7], v[56:63], v[124:127]
	v_mfma_f32_16x16x128_f8f6f4 v[120:123], v[8:15], v[56:63], v[120:123]
	v_mfma_f32_16x16x128_f8f6f4 v[108:111], v[0:7], v[48:55], v[108:111]
	v_mfma_f32_16x16x128_f8f6f4 v[104:107], v[8:15], v[48:55], v[104:107]
	v_mfma_f32_16x16x128_f8f6f4 v[92:95], v[0:7], v[40:47], v[92:95]
	v_mfma_f32_16x16x128_f8f6f4 v[88:91], v[8:15], v[40:47], v[88:91]
	v_mfma_f32_16x16x128_f8f6f4 v[76:79], v[0:7], v[32:39], v[76:79]
	v_mfma_f32_16x16x128_f8f6f4 v[72:75], v[8:15], v[32:39], v[72:75]
	s_barrier
	s_and_b64 vcc, exec, s[0:1]
	s_mov_b64 s[22:23], -1
	s_cbranch_vccnz .LBB4_20
	s_add_u32 s52, s46, 0x4100
	s_addc_u32 s13, s47, 0
	s_mov_b32 m0, s17
	s_and_b32 s53, s13, 0xffff
	s_mov_b32 s54, s14
	s_mov_b32 s55, s15
	buffer_load_dwordx4 v193, s[52:55], 0 offen lds
	s_mov_b32 m0, s31
	s_mov_b64 s[22:23], 0
	buffer_load_dwordx4 v195, s[52:55], 0 offen lds
	s_waitcnt vmcnt(10)

.LBB4_22:
	s_barrier
	v_mfma_f32_16x16x128_f8f6f4 v[116:119], v[24:31], v[56:63], v[116:119]
	v_add_u32_e32 v0, s45, v198
	v_add_u32_e32 v4, s45, v199
	v_mfma_f32_16x16x128_f8f6f4 v[112:115], v[16:23], v[56:63], v[112:115]
	v_mfma_f32_16x16x128_f8f6f4 v[100:103], v[24:31], v[48:55], v[100:103]
	v_mfma_f32_16x16x128_f8f6f4 v[96:99], v[16:23], v[48:55], v[96:99]
	v_mfma_f32_16x16x128_f8f6f4 v[84:87], v[24:31], v[40:47], v[84:87]
	v_mfma_f32_16x16x128_f8f6f4 v[80:83], v[16:23], v[40:47], v[80:83]
	v_mfma_f32_16x16x128_f8f6f4 v[68:71], v[24:31], v[32:39], v[68:71]
	v_mfma_f32_16x16x128_f8f6f4 v[64:67], v[16:23], v[32:39], v[64:67]
	s_barrier
	ds_read_b128 v[8:11], v0
	ds_read_b128 v[0:3], v0 offset:2048
	ds_read_b128 v[12:15], v4
	ds_read_b128 v[4:7], v4 offset:2048
	ds_read_b128 v[56:59], v200 offset:32768
	ds_read_b128 v[48:51], v200 offset:34816
	ds_read_b128 v[60:63], v201 offset:32768
	ds_read_b128 v[52:55], v201 offset:34816
	ds_read_b128 v[40:43], v200 offset:36864
	ds_read_b128 v[32:35], v200 offset:38912
	ds_read_b128 v[44:47], v201 offset:36864
	ds_read_b128 v[36:39], v201 offset:38912
	s_waitcnt vmcnt(8)
	s_and_b64 vcc, exec, s[0:1]
	s_cbranch_vccnz .LBB4_24
	s_add_u32 s52, s49, 0x40100
	s_addc_u32 s13, s50, 0
	s_and_b32 s53, s13, 0xffff
	s_mov_b32 s54, s14
	s_mov_b32 s55, s15
	s_mov_b32 m0, s34
	s_nop 0
	buffer_load_dwordx4 v192, s[52:55], 0 offen lds
	s_mov_b32 m0, s35
	s_nop 0
	buffer_load_dwordx4 v194, s[52:55], 0 offen lds
.LBB4_24:
	s_waitcnt lgkmcnt(8)
	s_barrier
	s_waitcnt lgkmcnt(0)
	v_mfma_f32_16x16x128_f8f6f4 v[188:191], v[8:15], v[56:63], v[188:191]
	v_mfma_f32_16x16x128_f8f6f4 v[184:187], v[0:7], v[56:63], v[184:187]
	v_mfma_f32_16x16x128_f8f6f4 v[172:175], v[8:15], v[48:55], v[172:175]
	v_mfma_f32_16x16x128_f8f6f4 v[168:171], v[0:7], v[48:55], v[168:171]
	v_mfma_f32_16x16x128_f8f6f4 v[156:159], v[8:15], v[40:47], v[156:159]
	v_mfma_f32_16x16x128_f8f6f4 v[152:155], v[0:7], v[40:47], v[152:155]
	v_mfma_f32_16x16x128_f8f6f4 v[140:143], v[8:15], v[32:39], v[140:143]
	v_mfma_f32_16x16x128_f8f6f4 v[136:139], v[0:7], v[32:39], v[136:139]
	s_barrier
	ds_read_b128 v[24:27], v207
	ds_read_b128 v[16:19], v207 offset:2048
	ds_read_b128 v[28:31], v208
	ds_read_b128 v[20:23], v208 offset:2048
	s_waitcnt vmcnt(8)
	s_and_b64 vcc, exec, s[0:1]
	s_cbranch_vccnz .LBB4_26
	s_and_b64 s[22:23], exec, s[18:19]
	s_cselect_b32 s20, s8, s20
	s_cselect_b32 s13, s3, s48
	s_add_u32 s48, s20, 0x80
	s_addc_u32 s13, s13, 0
	s_and_b32 s49, s13, 0xffff
	s_mov_b32 s50, s14
	s_mov_b32 s51, s15
	s_mov_b32 m0, s36
	s_nop 0
	buffer_load_dwordx4 v193, s[48:51], 0 offen lds
	s_mov_b32 m0, s37
	s_nop 0
	buffer_load_dwordx4 v195, s[48:51], 0 offen lds
.LBB4_26:
	s_barrier
	s_waitcnt lgkmcnt(0)
	v_mfma_f32_16x16x128_f8f6f4 v[180:183], v[24:31], v[56:63], v[180:183]
	v_mfma_f32_16x16x128_f8f6f4 v[176:179], v[16:23], v[56:63], v[176:179]
	v_mfma_f32_16x16x128_f8f6f4 v[164:167], v[24:31], v[48:55], v[164:167]
	v_mfma_f32_16x16x128_f8f6f4 v[160:163], v[16:23], v[48:55], v[160:163]
	v_mfma_f32_16x16x128_f8f6f4 v[148:151], v[24:31], v[40:47], v[148:151]
	v_mfma_f32_16x16x128_f8f6f4 v[144:147], v[16:23], v[40:47], v[144:147]
	v_mfma_f32_16x16x128_f8f6f4 v[132:135], v[24:31], v[32:39], v[132:135]
	v_mfma_f32_16x16x128_f8f6f4 v[128:131], v[16:23], v[32:39], v[128:131]
	s_barrier
	ds_read_b128 v[56:59], v200 offset:49152
	ds_read_b128 v[48:51], v200 offset:51200
	ds_read_b128 v[60:63], v201 offset:49152
	ds_read_b128 v[52:55], v201 offset:51200
	ds_read_b128 v[40:43], v200 offset:53248
	ds_read_b128 v[32:35], v200 offset:55296
	ds_read_b128 v[44:47], v201 offset:53248
	ds_read_b128 v[36:39], v201 offset:55296
	s_and_b64 vcc, exec, s[0:1]
	s_cbranch_vccnz .LBB4_28
	s_and_b64 s[18:19], exec, s[18:19]
	s_cselect_b32 s12, s16, s12
	s_cselect_b32 s13, s9, s21
	s_add_u32 s12, s12, 0x80
	s_addc_u32 s13, s13, 0
	s_and_b32 s13, s13, 0xffff
	s_mov_b32 m0, s38
	s_nop 0
	buffer_load_dwordx4 v192, s[12:15], 0 offen lds
	s_mov_b32 m0, s39
	s_nop 0
	buffer_load_dwordx4 v194, s[12:15], 0 offen lds
.LBB4_28:
	s_barrier
	s_waitcnt lgkmcnt(0)
	v_mfma_f32_16x16x128_f8f6f4 v[124:127], v[8:15], v[56:63], v[124:127]
	v_mfma_f32_16x16x128_f8f6f4 v[120:123], v[0:7], v[56:63], v[120:123]
	v_mfma_f32_16x16x128_f8f6f4 v[108:111], v[8:15], v[48:55], v[108:111]
	v_mfma_f32_16x16x128_f8f6f4 v[104:107], v[0:7], v[48:55], v[104:107]
	v_mfma_f32_16x16x128_f8f6f4 v[92:95], v[8:15], v[40:47], v[92:95]
	v_mfma_f32_16x16x128_f8f6f4 v[88:91], v[0:7], v[40:47], v[88:91]
	v_mfma_f32_16x16x128_f8f6f4 v[76:79], v[8:15], v[32:39], v[76:79]
	v_mfma_f32_16x16x128_f8f6f4 v[72:75], v[0:7], v[32:39], v[72:75]
	s_barrier
	s_and_b64 vcc, exec, s[0:1]
	s_cbranch_vccnz .LBB4_13
	s_add_u32 s12, s46, 0x4180
	s_addc_u32 s0, s47, 0
	s_and_b32 s13, s0, 0xffff
	s_mov_b32 m0, s40
	s_nop 0
	buffer_load_dwordx4 v193, s[12:15], 0 offen lds
	s_mov_b32 m0, s41
	s_nop 0
	buffer_load_dwordx4 v195, s[12:15], 0 offen lds
	s_branch .LBB4_13

.LBB5_16:
	s_and_b32 s35, s20, 3
	s_add_u32 s8, s12, 0x80
	s_load_dword s2, s[0:1], 0x48
	s_addc_u32 s0, s7, 0
	s_add_i32 s37, s25, 0x18000
	s_and_b32 s9, s0, 0xffff
	s_mov_b32 m0, s37
	s_add_i32 s38, s25, 0x1a000
	s_waitcnt vmcnt(4)
	s_barrier
	buffer_load_dwordx4 v192, s[8:11], 0 offen lds
	s_mov_b32 m0, s38
	v_lshrrev_b32_e32 v1, 4, v0
	buffer_load_dwordx4 v193, s[8:11], 0 offen lds
	s_add_u32 s8, s16, 0x80
	s_addc_u32 s0, s13, 0
	s_add_i32 s39, s25, 0x8000
	s_and_b32 s9, s0, 0xffff
	s_mov_b32 m0, s39
	s_add_i32 s40, s25, 0xa000
	buffer_load_dwordx4 v192, s[8:11], 0 offen lds
	s_mov_b32 m0, s40
	v_and_b32_e32 v194, 15, v0
	buffer_load_dwordx4 v193, s[8:11], 0 offen lds
	s_add_u32 s8, s12, 0x40080
	s_addc_u32 s0, s7, 0
	s_add_i32 s41, s25, 0x1c000
	s_and_b32 s9, s0, 0xffff
	s_mov_b32 m0, s41
	s_add_i32 s42, s25, 0x1e000
	buffer_load_dwordx4 v192, s[8:11], 0 offen lds
	s_mov_b32 m0, s42
	v_bfe_u32 v195, v0, 4, 2
	buffer_load_dwordx4 v193, s[8:11], 0 offen lds
	v_bfe_u32 v0, v0, 1, 3
	v_bitop3_b32 v0, v1, v0, 3 bitop3:0x6c
	v_lshlrev_b32_e32 v1, 7, v194
	v_lshlrev_b32_e32 v0, 4, v0
	v_lshl_or_b32 v2, s3, 13, v1
	v_lshl_or_b32 v1, s35, 12, v1
	s_waitcnt vmcnt(6)
	v_or_b32_e32 v3, v2, v0
	v_or_b32_e32 v196, v1, v0
	v_bitop3_b32 v2, v2, 64, v0 bitop3:0x36
	v_bitop3_b32 v197, v1, 64, v0 bitop3:0x36
	v_mov_b32_e32 v64, 0
	s_add_i32 s0, 0, 0x10000
	s_add_i32 s1, 0, 0x14000
	s_add_i32 s43, s25, 0xc000
	s_add_i32 s44, s25, 0xe000
	s_mov_b32 s45, -2
	s_mov_b64 s[14:15], 0
	v_add_u32_e32 v198, 0, v3
	v_add_u32_e32 v199, 0, v2
	s_add_i32 s46, 0, 0x18000
	v_mov_b32_e32 v65, v64
	v_mov_b32_e32 v66, v64
	v_mov_b32_e32 v67, v64
	v_mov_b32_e32 v68, v64
	v_mov_b32_e32 v69, v64
	v_mov_b32_e32 v70, v64
	v_mov_b32_e32 v71, v64
	v_mov_b32_e32 v76, v64
	v_mov_b32_e32 v77, v64
	v_mov_b32_e32 v78, v64
	v_mov_b32_e32 v79, v64
	v_mov_b32_e32 v80, v64
	v_mov_b32_e32 v81, v64
	v_mov_b32_e32 v82, v64
	v_mov_b32_e32 v83, v64
	v_mov_b32_e32 v88, v64
	v_mov_b32_e32 v89, v64
	v_mov_b32_e32 v90, v64
	v_mov_b32_e32 v91, v64
	v_mov_b32_e32 v92, v64
	v_mov_b32_e32 v93, v64
	v_mov_b32_e32 v94, v64
	v_mov_b32_e32 v95, v64
	v_mov_b32_e32 v104, v64
	v_mov_b32_e32 v105, v64
	v_mov_b32_e32 v106, v64
	v_mov_b32_e32 v107, v64
	v_mov_b32_e32 v108, v64
	v_mov_b32_e32 v109, v64
	v_mov_b32_e32 v110, v64
	v_mov_b32_e32 v111, v64
	v_mov_b32_e32 v72, v64
	v_mov_b32_e32 v73, v64
	v_mov_b32_e32 v74, v64
	v_mov_b32_e32 v75, v64
	v_mov_b32_e32 v84, v64
	v_mov_b32_e32 v85, v64
	v_mov_b32_e32 v86, v64
	v_mov_b32_e32 v87, v64
	v_mov_b32_e32 v96, v64
	v_mov_b32_e32 v97, v64
	v_mov_b32_e32 v98, v64
	v_mov_b32_e32 v99, v64
	v_mov_b32_e32 v100, v64
	v_mov_b32_e32 v101, v64
	v_mov_b32_e32 v102, v64
	v_mov_b32_e32 v103, v64
	v_mov_b32_e32 v112, v64
	v_mov_b32_e32 v113, v64
	v_mov_b32_e32 v114, v64
	v_mov_b32_e32 v115, v64
	v_mov_b32_e32 v116, v64
	v_mov_b32_e32 v117, v64
	v_mov_b32_e32 v118, v64
	v_mov_b32_e32 v119, v64
	v_mov_b32_e32 v120, v64
	v_mov_b32_e32 v121, v64
	v_mov_b32_e32 v122, v64
	v_mov_b32_e32 v123, v64
	v_mov_b32_e32 v124, v64
	v_mov_b32_e32 v125, v64
	v_mov_b32_e32 v126, v64
	v_mov_b32_e32 v127, v64
	v_mov_b32_e32 v128, v64
	v_mov_b32_e32 v129, v64
	v_mov_b32_e32 v130, v64
	v_mov_b32_e32 v131, v64
	v_mov_b32_e32 v132, v64
	v_mov_b32_e32 v133, v64
	v_mov_b32_e32 v134, v64
	v_mov_b32_e32 v135, v64
	v_mov_b32_e32 v140, v64
	v_mov_b32_e32 v141, v64
	v_mov_b32_e32 v142, v64
	v_mov_b32_e32 v143, v64
	v_mov_b32_e32 v148, v64
	v_mov_b32_e32 v149, v64
	v_mov_b32_e32 v150, v64
	v_mov_b32_e32 v151, v64
	v_mov_b32_e32 v156, v64
	v_mov_b32_e32 v157, v64
	v_mov_b32_e32 v158, v64
	v_mov_b32_e32 v159, v64
	v_mov_b32_e32 v164, v64
	v_mov_b32_e32 v165, v64
	v_mov_b32_e32 v166, v64
	v_mov_b32_e32 v167, v64
	v_mov_b32_e32 v172, v64
	v_mov_b32_e32 v173, v64
	v_mov_b32_e32 v174, v64
	v_mov_b32_e32 v175, v64
	v_mov_b32_e32 v180, v64
	v_mov_b32_e32 v181, v64
	v_mov_b32_e32 v182, v64
	v_mov_b32_e32 v183, v64
	v_mov_b32_e32 v136, v64
	v_mov_b32_e32 v137, v64
	v_mov_b32_e32 v138, v64
	v_mov_b32_e32 v139, v64
	v_mov_b32_e32 v144, v64
	v_mov_b32_e32 v145, v64
	v_mov_b32_e32 v146, v64
	v_mov_b32_e32 v147, v64
	v_mov_b32_e32 v152, v64
	v_mov_b32_e32 v153, v64
	v_mov_b32_e32 v154, v64
	v_mov_b32_e32 v155, v64
	v_mov_b32_e32 v160, v64
	v_mov_b32_e32 v161, v64
	v_mov_b32_e32 v162, v64
	v_mov_b32_e32 v163, v64
	v_mov_b32_e32 v168, v64
	v_mov_b32_e32 v169, v64
	v_mov_b32_e32 v170, v64
	v_mov_b32_e32 v171, v64
	v_mov_b32_e32 v176, v64
	v_mov_b32_e32 v177, v64
	v_mov_b32_e32 v178, v64
	v_mov_b32_e32 v179, v64
	v_mov_b32_e32 v184, v64
	v_mov_b32_e32 v185, v64
	v_mov_b32_e32 v186, v64
	v_mov_b32_e32 v187, v64
	v_mov_b32_e32 v188, v64
	v_mov_b32_e32 v189, v64
	v_mov_b32_e32 v190, v64
	v_mov_b32_e32 v191, v64
	v_add_u32_e32 v200, s0, v196
	v_add_u32_e32 v201, s0, v197
	v_add_u32_e32 v202, s1, v196
	v_add_u32_e32 v203, s1, v197
	s_barrier
	s_cmpk_eq_i32 s14, 0x700
	s_cselect_b64 s[18:19], -1, 0
	s_cmpk_lg_i32 s14, 0x700
	s_cselect_b64 s[26:27], -1, 0
	s_add_u32 s50, s16, s14
	s_addc_u32 s51, s13, s15
	s_add_u32 s47, s12, s14
	s_addc_u32 s48, s7, s15
	s_add_u32 s20, s47, 0x100
	s_addc_u32 s49, s48, 0
	s_add_u32 s8, s50, 0x40080
	s_addc_u32 s0, s51, 0
	s_and_b32 s9, s0, 0xffff
	v_add_u32_e32 v205, 0x1c000, v196
	v_add_u32_e32 v206, 0x1c000, v197
	s_cmpk_lt_u32 s28, 0x100
	s_cbranch_scc1 .Lp4_prio_done
	s_setprio 1

.LBB5_17:
	s_waitcnt vmcnt(10)
	s_barrier
	v_mfma_f32_16x16x128_f8f6f4 v[108:111], v[24:31], v[56:63], v[108:111]
	s_add_i32 s45, s45, 2
	s_add_u32 s14, s14, 0x100
	s_addc_u32 s15, s15, 0
	v_mfma_f32_16x16x128_f8f6f4 v[104:107], v[16:23], v[56:63], v[104:107]
	s_cmpk_eq_i32 s14, 0x700
	s_cselect_b64 s[18:19], -1, 0
	s_cmpk_lg_i32 s14, 0x700
	s_cselect_b64 s[26:27], -1, 0
	v_mfma_f32_16x16x128_f8f6f4 v[92:95], v[24:31], v[48:55], v[92:95]
	s_add_u32 s50, s16, s14
	s_addc_u32 s51, s13, s15
	s_add_u32 s47, s12, s14
	s_addc_u32 s48, s7, s15
	v_mfma_f32_16x16x128_f8f6f4 v[88:91], v[16:23], v[48:55], v[88:91]
	s_add_u32 s20, s47, 0x100
	s_addc_u32 s49, s48, 0
	s_add_u32 s8, s50, 0x40080
	s_addc_u32 s0, s51, 0
	v_mfma_f32_16x16x128_f8f6f4 v[80:83], v[24:31], v[40:47], v[80:83]
	s_and_b32 s9, s0, 0xffff
	s_cmp_gt_u32 s45, 13
	v_mfma_f32_16x16x128_f8f6f4 v[76:79], v[16:23], v[40:47], v[76:79]
	v_mfma_f32_16x16x128_f8f6f4 v[68:71], v[24:31], v[32:39], v[68:71]
	v_mfma_f32_16x16x128_f8f6f4 v[64:67], v[16:23], v[32:39], v[64:67]
	s_barrier
	s_cbranch_scc1 .LBB5_34
.LBB5_18:
	ds_read_b128 v[0:3], v200
	ds_read_b128 v[8:11], v200 offset:2048
	ds_read_b128 v[4:7], v201
	ds_read_b128 v[12:15], v201 offset:2048
	s_mov_b32 m0, s43
	ds_read_b128 v[56:59], v198
	ds_read_b128 v[48:51], v198 offset:2048
	ds_read_b128 v[60:63], v199
	ds_read_b128 v[52:55], v199 offset:2048
	ds_read_b128 v[40:43], v198 offset:4096
	ds_read_b128 v[32:35], v198 offset:6144
	ds_read_b128 v[44:47], v199 offset:4096
	ds_read_b128 v[36:39], v199 offset:6144
	s_waitcnt vmcnt(8)
	buffer_load_dwordx4 v192, s[8:11], 0 offen lds
	s_mov_b32 m0, s44
	s_nop 0
	buffer_load_dwordx4 v193, s[8:11], 0 offen lds
	s_waitcnt lgkmcnt(8)
	s_barrier
	s_waitcnt lgkmcnt(0)
	v_mfma_f32_16x16x128_f8f6f4 v[188:191], v[0:7], v[56:63], v[188:191]
	v_mfma_f32_16x16x128_f8f6f4 v[184:187], v[8:15], v[56:63], v[184:187]
	v_mfma_f32_16x16x128_f8f6f4 v[176:179], v[0:7], v[48:55], v[176:179]
	v_mfma_f32_16x16x128_f8f6f4 v[168:171], v[8:15], v[48:55], v[168:171]
	v_mfma_f32_16x16x128_f8f6f4 v[160:163], v[0:7], v[40:47], v[160:163]
	v_mfma_f32_16x16x128_f8f6f4 v[152:155], v[8:15], v[40:47], v[152:155]
	v_mfma_f32_16x16x128_f8f6f4 v[144:147], v[0:7], v[32:39], v[144:147]
	v_mfma_f32_16x16x128_f8f6f4 v[136:139], v[8:15], v[32:39], v[136:139]
	s_barrier
	ds_read_b128 v[24:27], v202
	ds_read_b128 v[16:19], v202 offset:2048
	ds_read_b128 v[28:31], v203
	ds_read_b128 v[20:23], v203 offset:2048
	s_waitcnt vmcnt(8)
	s_and_b64 vcc, exec, s[18:19]
	s_cbranch_vccnz .LBB5_20
	s_and_b32 s21, s49, 0xffff
	s_mov_b32 s22, s10
	s_mov_b32 s23, s11
	s_mov_b32 m0, s29
	s_nop 0
	buffer_load_dwordx4 v192, s[20:23], 0 offen lds
	s_mov_b32 m0, s30
	s_nop 0
	buffer_load_dwordx4 v193, s[20:23], 0 offen lds
.LBB5_20:
	s_barrier
	s_waitcnt lgkmcnt(0)
	v_mfma_f32_16x16x128_f8f6f4 v[180:183], v[24:31], v[56:63], v[180:183]
	s_add_u32 s8, s50, 0x100
	s_addc_u32 s21, s51, 0
	v_mfma_f32_16x16x128_f8f6f4 v[172:175], v[16:23], v[56:63], v[172:175]
	v_mfma_f32_16x16x128_f8f6f4 v[164:167], v[24:31], v[48:55], v[164:167]
	v_mfma_f32_16x16x128_f8f6f4 v[156:159], v[16:23], v[48:55], v[156:159]
	v_mfma_f32_16x16x128_f8f6f4 v[148:151], v[24:31], v[40:47], v[148:151]
	v_mfma_f32_16x16x128_f8f6f4 v[140:143], v[16:23], v[40:47], v[140:143]
	v_mfma_f32_16x16x128_f8f6f4 v[132:135], v[24:31], v[32:39], v[132:135]
	v_mfma_f32_16x16x128_f8f6f4 v[128:131], v[16:23], v[32:39], v[128:131]
	s_barrier
	ds_read_b128 v[56:59], v198 offset:16384
	ds_read_b128 v[48:51], v198 offset:18432
	ds_read_b128 v[60:63], v199 offset:16384
	ds_read_b128 v[52:55], v199 offset:18432
	ds_read_b128 v[40:43], v198 offset:20480
	ds_read_b128 v[32:35], v198 offset:22528
	ds_read_b128 v[44:47], v199 offset:20480
	ds_read_b128 v[36:39], v199 offset:22528
	v_cndmask_b32_e64 v204, 0, 1, s[26:27]
	v_cmp_ne_u32_e64 s[0:1], 1, v204
	s_andn2_b64 vcc, exec, s[26:27]
	s_cbranch_vccnz .LBB5_22
	s_and_b32 s9, s21, 0xffff
	s_mov_b32 m0, s25
	s_nop 0
	buffer_load_dwordx4 v192, s[8:11], 0 offen lds
	s_mov_b32 m0, s31
	s_nop 0
	buffer_load_dwordx4 v193, s[8:11], 0 offen lds
.LBB5_22:
	s_barrier
	s_waitcnt lgkmcnt(0)
	v_mfma_f32_16x16x128_f8f6f4 v[124:127], v[0:7], v[56:63], v[124:127]
	v_mfma_f32_16x16x128_f8f6f4 v[120:123], v[8:15], v[56:63], v[120:123]
	v_mfma_f32_16x16x128_f8f6f4 v[116:119], v[0:7], v[48:55], v[116:119]
	v_mfma_f32_16x16x128_f8f6f4 v[112:115], v[8:15], v[48:55], v[112:115]
	v_mfma_f32_16x16x128_f8f6f4 v[100:103], v[0:7], v[40:47], v[100:103]
	v_mfma_f32_16x16x128_f8f6f4 v[96:99], v[8:15], v[40:47], v[96:99]
	v_mfma_f32_16x16x128_f8f6f4 v[84:87], v[0:7], v[32:39], v[84:87]
	v_mfma_f32_16x16x128_f8f6f4 v[72:75], v[8:15], v[32:39], v[72:75]
	s_barrier
	s_and_b64 vcc, exec, s[0:1]
	s_mov_b64 s[22:23], -1
	s_cbranch_vccnz .LBB5_24
	s_add_u32 s52, s47, 0x40100
	s_addc_u32 s9, s48, 0
	s_mov_b32 m0, s17
	s_and_b32 s53, s9, 0xffff
	s_mov_b32 s54, s10
	s_mov_b32 s55, s11
	buffer_load_dwordx4 v192, s[52:55], 0 offen lds
	s_mov_b32 m0, s33
	s_mov_b64 s[22:23], 0
	buffer_load_dwordx4 v193, s[52:55], 0 offen lds
	s_waitcnt vmcnt(10)

.LBB5_26:
	s_barrier
	v_mfma_f32_16x16x128_f8f6f4 v[108:111], v[24:31], v[56:63], v[108:111]
	v_add_u32_e32 v0, s46, v196
	v_add_u32_e32 v4, s46, v197
	v_mfma_f32_16x16x128_f8f6f4 v[104:107], v[16:23], v[56:63], v[104:107]
	v_mfma_f32_16x16x128_f8f6f4 v[92:95], v[24:31], v[48:55], v[92:95]
	v_mfma_f32_16x16x128_f8f6f4 v[88:91], v[16:23], v[48:55], v[88:91]
	v_mfma_f32_16x16x128_f8f6f4 v[80:83], v[24:31], v[40:47], v[80:83]
	v_mfma_f32_16x16x128_f8f6f4 v[76:79], v[16:23], v[40:47], v[76:79]
	v_mfma_f32_16x16x128_f8f6f4 v[68:71], v[24:31], v[32:39], v[68:71]
	v_mfma_f32_16x16x128_f8f6f4 v[64:67], v[16:23], v[32:39], v[64:67]
	s_barrier
	ds_read_b128 v[8:11], v0
	ds_read_b128 v[0:3], v0 offset:2048
	ds_read_b128 v[12:15], v4
	ds_read_b128 v[4:7], v4 offset:2048
	ds_read_b128 v[56:59], v198 offset:32768
	ds_read_b128 v[48:51], v198 offset:34816
	ds_read_b128 v[60:63], v199 offset:32768
	ds_read_b128 v[52:55], v199 offset:34816
	ds_read_b128 v[40:43], v198 offset:36864
	ds_read_b128 v[32:35], v198 offset:38912
	ds_read_b128 v[44:47], v199 offset:36864
	ds_read_b128 v[36:39], v199 offset:38912
	s_waitcnt vmcnt(8)
	s_and_b64 vcc, exec, s[0:1]
	s_cbranch_vccnz .LBB5_28
	s_add_u32 s52, s50, 0x40100
	s_addc_u32 s9, s51, 0
	s_and_b32 s53, s9, 0xffff
	s_mov_b32 s54, s10
	s_mov_b32 s55, s11
	s_mov_b32 m0, s34
	s_nop 0
	buffer_load_dwordx4 v192, s[52:55], 0 offen lds
	s_mov_b32 m0, s36
	s_nop 0
	buffer_load_dwordx4 v193, s[52:55], 0 offen lds
.LBB5_28:
	s_waitcnt lgkmcnt(8)
	s_barrier
	s_waitcnt lgkmcnt(0)
	v_mfma_f32_16x16x128_f8f6f4 v[188:191], v[8:15], v[56:63], v[188:191]
	v_mfma_f32_16x16x128_f8f6f4 v[184:187], v[0:7], v[56:63], v[184:187]
	v_mfma_f32_16x16x128_f8f6f4 v[176:179], v[8:15], v[48:55], v[176:179]
	v_mfma_f32_16x16x128_f8f6f4 v[168:171], v[0:7], v[48:55], v[168:171]
	v_mfma_f32_16x16x128_f8f6f4 v[160:163], v[8:15], v[40:47], v[160:163]
	v_mfma_f32_16x16x128_f8f6f4 v[152:155], v[0:7], v[40:47], v[152:155]
	v_mfma_f32_16x16x128_f8f6f4 v[144:147], v[8:15], v[32:39], v[144:147]
	v_mfma_f32_16x16x128_f8f6f4 v[136:139], v[0:7], v[32:39], v[136:139]
	s_barrier
	ds_read_b128 v[24:27], v205
	ds_read_b128 v[16:19], v205 offset:2048
	ds_read_b128 v[28:31], v206
	ds_read_b128 v[20:23], v206 offset:2048
	s_waitcnt vmcnt(8)
	s_and_b64 vcc, exec, s[0:1]
	s_cbranch_vccnz .LBB5_30
	s_and_b64 s[22:23], exec, s[18:19]
	s_cselect_b32 s20, s12, s20
	s_cselect_b32 s9, s7, s49
	s_add_u32 s52, s20, 0x80
	s_addc_u32 s9, s9, 0
	s_and_b32 s53, s9, 0xffff
	s_mov_b32 s54, s10
	s_mov_b32 s55, s11
	s_mov_b32 m0, s37
	s_nop 0
	buffer_load_dwordx4 v192, s[52:55], 0 offen lds
	s_mov_b32 m0, s38
	s_nop 0
	buffer_load_dwordx4 v193, s[52:55], 0 offen lds
.LBB5_30:
	s_barrier
	s_waitcnt lgkmcnt(0)
	v_mfma_f32_16x16x128_f8f6f4 v[180:183], v[24:31], v[56:63], v[180:183]
	v_mfma_f32_16x16x128_f8f6f4 v[172:175], v[16:23], v[56:63], v[172:175]
	v_mfma_f32_16x16x128_f8f6f4 v[164:167], v[24:31], v[48:55], v[164:167]
	v_mfma_f32_16x16x128_f8f6f4 v[156:159], v[16:23], v[48:55], v[156:159]
	v_mfma_f32_16x16x128_f8f6f4 v[148:151], v[24:31], v[40:47], v[148:151]
	v_mfma_f32_16x16x128_f8f6f4 v[140:143], v[16:23], v[40:47], v[140:143]
	v_mfma_f32_16x16x128_f8f6f4 v[132:135], v[24:31], v[32:39], v[132:135]
	v_mfma_f32_16x16x128_f8f6f4 v[128:131], v[16:23], v[32:39], v[128:131]
	s_barrier
	ds_read_b128 v[56:59], v198 offset:49152
	ds_read_b128 v[48:51], v198 offset:51200
	ds_read_b128 v[60:63], v199 offset:49152
	ds_read_b128 v[52:55], v199 offset:51200
	ds_read_b128 v[40:43], v198 offset:53248
	ds_read_b128 v[32:35], v198 offset:55296
	ds_read_b128 v[44:47], v199 offset:53248
	ds_read_b128 v[36:39], v199 offset:55296
	s_and_b64 vcc, exec, s[0:1]
	s_cbranch_vccnz .LBB5_32
	s_and_b64 s[18:19], exec, s[18:19]
	s_cselect_b32 s8, s16, s8
	s_cselect_b32 s9, s13, s21
	s_add_u32 s8, s8, 0x80
	s_addc_u32 s9, s9, 0
	s_and_b32 s9, s9, 0xffff
	s_mov_b32 m0, s39
	s_nop 0
	buffer_load_dwordx4 v192, s[8:11], 0 offen lds
	s_mov_b32 m0, s40
	s_nop 0
	buffer_load_dwordx4 v193, s[8:11], 0 offen lds
.LBB5_32:
	s_barrier
	s_waitcnt lgkmcnt(0)
	v_mfma_f32_16x16x128_f8f6f4 v[124:127], v[8:15], v[56:63], v[124:127]
	v_mfma_f32_16x16x128_f8f6f4 v[120:123], v[0:7], v[56:63], v[120:123]
	v_mfma_f32_16x16x128_f8f6f4 v[116:119], v[8:15], v[48:55], v[116:119]
	v_mfma_f32_16x16x128_f8f6f4 v[112:115], v[0:7], v[48:55], v[112:115]
	v_mfma_f32_16x16x128_f8f6f4 v[100:103], v[8:15], v[40:47], v[100:103]
	v_mfma_f32_16x16x128_f8f6f4 v[96:99], v[0:7], v[40:47], v[96:99]
	v_mfma_f32_16x16x128_f8f6f4 v[84:87], v[8:15], v[32:39], v[84:87]
	v_mfma_f32_16x16x128_f8f6f4 v[72:75], v[0:7], v[32:39], v[72:75]
	s_barrier
	s_and_b64 vcc, exec, s[0:1]
	s_cbranch_vccnz .LBB5_17
	s_add_u32 s8, s47, 0x40180
	s_addc_u32 s0, s48, 0
	s_and_b32 s9, s0, 0xffff
	s_mov_b32 m0, s41
	s_nop 0
	buffer_load_dwordx4 v192, s[8:11], 0 offen lds
	s_mov_b32 m0, s42
	s_nop 0
	buffer_load_dwordx4 v193, s[8:11], 0 offen lds
	s_branch .LBB5_17
